# RMSNorm phases: wave_sum/wave_max ds_bpermute butterflies -> DPP (12 phases)
# baseline (speedup 1.0000x reference)
; __device__ __forceinline__ float wave_sum(float v) {
; #pragma unroll
;     for (int o = 1; o < 64; o <<= 1) v += __shfl_xor(v, o);
;     return v;
; }
;     ...
;             f32x4 v[8]; float ss = 0.f; load_row<SB>(xin, (size_t)row, lane, v);
; #pragma unroll
;             for (int q = 0; q < 8; ++q) ss += (v[q].x * v[q].x + v[q].y * v[q].y) + (v[q].z * v[q].z + v[q].w * v[q].w);
;             const float rstd = 1.0f / sqrtf(wave_sum(ss) * (1.0f / DM) + NORM_EPS);
;             if (F8 == 2) { unsigned* o4 = (unsigned*)((unsigned char*)xn + (size_t)row * DM) + lane; float mx = 0.f;
; #pragma unroll
;                 for (int q = 0; q < 8; ++q) { v[q] = v[q] * rstd * gn[q]; mx = fmaxf(fmaxf(mx, fmaxf(fabsf(v[q].x), fabsf(v[q].y))), fmaxf(fabsf(v[q].z), fabsf(v[q].w))); }
.LBB0_151:
	global_load_dwordx4 v[42:45], v[50:51], off offset:-2048
	global_load_dwordx4 v[34:37], v[50:51], off
	global_load_dwordx4 v[38:41], v[50:51], off offset:-1024
	global_load_dwordx4 v[68:71], v[50:51], off offset:-3072
	v_add_co_u32_e32 v88, vcc, 0xfffff000, v50
	s_waitcnt vmcnt(0)
	v_pk_mul_f32 v[90:91], v[42:43], v[42:43]
	v_addc_co_u32_e32 v89, vcc, -1, v51, vcc
	global_load_dwordx4 v[72:75], v[88:89], off offset:-1024
	global_load_dwordx4 v[76:79], v[88:89], off offset:-3072
	global_load_dwordx4 v[80:83], v[88:89], off offset:-2048
	global_load_dwordx4 v[84:87], v[50:51], off offset:-4096
	v_pk_mul_f32 v[88:89], v[44:45], v[44:45]
	v_mul_f32_e32 v92, v39, v39
	v_mul_f32_e32 v94, v41, v41
	v_mul_f32_e32 v67, v36, v36
	v_mul_f32_e32 v98, v37, v37
	v_pk_mov_b32 v[96:97], v[90:91], v[88:89] op_sel:[1,0]
	v_mov_b32_e32 v91, v89
	v_pk_fma_f32 v[88:89], v[38:39], v[38:39], v[92:93] op_sel_hi:[1,1,0]
	v_pk_fma_f32 v[92:93], v[40:41], v[40:41], v[94:95] op_sel_hi:[1,1,0]
	v_pk_add_f32 v[90:91], v[96:97], v[90:91]
	v_mov_b32_e32 v89, v67
	v_mov_b32_e32 v93, v98
	v_pk_add_f32 v[88:89], v[88:89], v[92:93]
	v_mul_f32_e32 v107, v70, v70
	v_mul_f32_e32 v109, v71, v71
	v_mul_f32_e32 v112, v69, v69
	v_mul_f32_e32 v113, v68, v68
	v_mul_f32_e32 v114, v35, v35
	v_mul_f32_e32 v115, v34, v34
	v_pk_add_f32 v[90:91], v[90:91], v[90:91] op_sel:[0,1] op_sel_hi:[1,0]
	s_waitcnt vmcnt(3)
	v_pk_mul_f32 v[94:95], v[74:75], v[74:75]
	v_pk_mul_f32 v[96:97], v[72:73], v[72:73]
	s_waitcnt vmcnt(2)
	v_mov_b32_e32 v100, v77
	s_waitcnt vmcnt(1)
	v_mov_b32_e32 v101, v81
	v_mov_b32_e32 v104, v79
	v_mov_b32_e32 v105, v83
	v_mov_b32_e32 v98, v76
	v_mov_b32_e32 v99, v80
	v_mov_b32_e32 v102, v78
	v_mov_b32_e32 v103, v82
	v_pk_mov_b32 v[110:111], v[96:97], v[94:95] op_sel:[1,0]
	v_mov_b32_e32 v97, v95
	v_pk_mul_f32 v[92:93], v[100:101], v[100:101]
	v_pk_mul_f32 v[94:95], v[104:105], v[104:105]
	v_pk_fma_f32 v[92:93], v[98:99], v[98:99], v[92:93]
	v_pk_fma_f32 v[94:95], v[102:103], v[102:103], v[94:95]
	s_waitcnt vmcnt(0)
	v_mul_f32_e32 v106, v85, v85
	v_mul_f32_e32 v108, v87, v87
	v_pk_add_f32 v[96:97], v[110:111], v[96:97]
	v_pk_add_f32 v[92:93], v[92:93], v[94:95]
	v_pk_fma_f32 v[100:101], v[84:85], v[84:85], v[106:107] op_sel_hi:[1,1,0]
	v_pk_fma_f32 v[104:105], v[86:87], v[86:87], v[108:109] op_sel_hi:[1,1,0]
	v_pk_add_f32 v[96:97], v[96:97], v[96:97] op_sel:[0,1] op_sel_hi:[1,0]
	v_pk_add_f32 v[92:93], v[92:93], v[92:93] op_sel:[0,1] op_sel_hi:[1,0]
	v_mov_b32_e32 v101, v107
	v_mov_b32_e32 v105, v109
	v_mov_b32_e32 v97, v112
	v_mov_b32_e32 v93, v113
	v_pk_add_f32 v[94:95], v[100:101], v[104:105]
	v_pk_add_f32 v[92:93], v[92:93], v[96:97]
	v_mov_b32_e32 v91, v114
	v_pk_add_f32 v[92:93], v[92:93], v[94:95]
	s_nop 0
	v_pk_add_f32 v[92:93], v[92:93], v[92:93] op_sel:[0,1] op_sel_hi:[1,0]
	s_nop 0
	v_mov_b32_e32 v93, v115
	v_pk_add_f32 v[90:91], v[92:93], v[90:91]
	s_nop 0
	v_pk_add_f32 v[88:89], v[90:91], v[88:89]
	s_nop 0
	v_add_f32_e32 v67, v88, v89
	s_nop 0
	s_waitcnt lgkmcnt(0)
	s_nop 1
	v_add_f32_dpp v67, v67, v67 quad_perm:[1,0,3,2] row_mask:0xf bank_mask:0xf bound_ctrl:1
	s_nop 0
	s_waitcnt lgkmcnt(0)
	s_nop 1
	v_add_f32_dpp v67, v67, v67 quad_perm:[2,3,0,1] row_mask:0xf bank_mask:0xf bound_ctrl:1
	s_nop 0
	s_waitcnt lgkmcnt(0)
	s_nop 1
	v_add_f32_dpp v67, v67, v67 row_half_mirror row_mask:0xf bank_mask:0xf bound_ctrl:1
	s_nop 0
	s_waitcnt lgkmcnt(0)
	s_nop 1
	v_add_f32_dpp v67, v67, v67 row_mirror row_mask:0xf bank_mask:0xf bound_ctrl:1
	s_nop 0
	s_waitcnt lgkmcnt(0)
	s_nop 1
	v_add_f32_dpp v67, v67, v67 row_bcast:15 row_mask:0xa bank_mask:0xf
	s_nop 0
	s_waitcnt lgkmcnt(0)
	s_nop 1
	v_add_f32_dpp v67, v67, v67 row_bcast:31 row_mask:0xc bank_mask:0xf
	s_nop 0
	v_readlane_b32 s98, v67, 63
	s_nop 1
	v_mov_b32_e32 v67, s98
	v_fmamk_f32 v67, v67, 0x3a000000, v65
	v_mul_f32_e32 v88, 0x4f800000, v67
	v_cmp_gt_f32_e32 vcc, s7, v67
	s_nop 1
	v_cndmask_b32_e32 v67, v67, v88, vcc
	v_sqrt_f32_e32 v88, v67
	s_nop 0
	v_add_u32_e32 v89, -1, v88
	v_add_u32_e32 v90, 1, v88
	v_fma_f32 v91, -v89, v88, v67
	v_fma_f32 v92, -v90, v88, v67
	v_cmp_ge_f32_e64 s[2:3], 0, v91
	s_nop 1
	v_cndmask_b32_e64 v88, v88, v89, s[2:3]
	v_cmp_lt_f32_e64 s[2:3], 0, v92
	s_nop 1
	v_cndmask_b32_e64 v88, v88, v90, s[2:3]
	v_mul_f32_e32 v89, 0x37800000, v88
	v_cndmask_b32_e32 v88, v88, v89, vcc
	v_cmp_class_f32_e32 vcc, v67, v66
	s_nop 1
	v_cndmask_b32_e32 v67, v88, v67, vcc
	v_div_scale_f32 v88, s[2:3], v67, v67, 1.0
	v_rcp_f32_e32 v89, v88
	v_div_scale_f32 v90, vcc, 1.0, v67, 1.0
	v_fma_f32 v91, -v88, v89, 1.0
	v_fmac_f32_e32 v89, v91, v89
	v_mul_f32_e32 v91, v90, v89
	v_fma_f32 v92, -v88, v91, v90
	v_fmac_f32_e32 v91, v92, v89
	v_fma_f32 v88, -v88, v91, v90
	v_div_fmas_f32 v88, v88, v89, v91
	v_div_fixup_f32 v88, v88, v67, 1.0
	v_pk_mul_f32 v[76:77], v[76:77], v[88:89] op_sel_hi:[1,0]
	v_pk_mul_f32 v[78:79], v[78:79], v[88:89] op_sel_hi:[1,0]
	v_pk_mul_f32 v[80:81], v[80:81], v[88:89] op_sel_hi:[1,0]
	v_pk_mul_f32 v[82:83], v[82:83], v[88:89] op_sel_hi:[1,0]
	v_pk_mul_f32 v[34:35], v[34:35], v[88:89] op_sel_hi:[1,0]
	v_pk_mul_f32 v[78:79], v[4:5], v[78:79]
	v_pk_mul_f32 v[76:77], v[2:3], v[76:77]
	v_pk_mul_f32 v[72:73], v[72:73], v[88:89] op_sel_hi:[1,0]
	v_pk_mul_f32 v[74:75], v[74:75], v[88:89] op_sel_hi:[1,0]
	v_pk_mul_f32 v[84:85], v[84:85], v[88:89] op_sel_hi:[1,0]
	v_pk_mul_f32 v[86:87], v[86:87], v[88:89] op_sel_hi:[1,0]
	v_pk_mul_f32 v[68:69], v[68:69], v[88:89] op_sel_hi:[1,0]
	v_pk_mul_f32 v[70:71], v[70:71], v[88:89] op_sel_hi:[1,0]
	v_pk_mul_f32 v[42:43], v[42:43], v[88:89] op_sel_hi:[1,0]
	v_pk_mul_f32 v[44:45], v[44:45], v[88:89] op_sel_hi:[1,0]
	v_pk_mul_f32 v[38:39], v[38:39], v[88:89] op_sel_hi:[1,0]
; __device__ __forceinline__ float wave_max(float v) {
; #pragma unroll
;     for (int o = 1; o < 64; o <<= 1) v = fmaxf(v, __shfl_xor(v, o));
;     return v;
; }
;     ...
;                 for (int q = 0; q < 8; ++q) { v[q] = v[q] * rstd * gn[q]; mx = fmaxf(fmaxf(mx, fmaxf(fabsf(v[q].x), fabsf(v[q].y))), fmaxf(fabsf(v[q].z), fabsf(v[q].w))); }
;                 mx = fmaxf(wave_max(mx), 1e-30f); const float qs = 127.0f / mx;
	v_pk_mul_f32 v[40:41], v[40:41], v[88:89] op_sel_hi:[1,0]
	v_pk_mul_f32 v[36:37], v[36:37], v[88:89] op_sel_hi:[1,0]
	v_pk_mul_f32 v[82:83], v[8:9], v[82:83]
	v_pk_mul_f32 v[80:81], v[6:7], v[80:81]
	v_pk_mul_f32 v[88:89], v[30:31], v[34:35]
	v_max_f32_e64 v34, |v76|, |v77|
	v_max_f32_e64 v35, |v78|, |v79|
	v_pk_mul_f32 v[74:75], v[12:13], v[74:75]
	v_pk_mul_f32 v[72:73], v[10:11], v[72:73]
	v_max_f32_e64 v67, |v80|, |v81|
	v_max_f32_e64 v90, |v82|, |v83|
	v_max3_f32 v34, v34, 0, v35
	v_pk_mul_f32 v[86:87], v[16:17], v[86:87]
	v_pk_mul_f32 v[84:85], v[14:15], v[84:85]
	v_max_f32_e64 v91, |v72|, |v73|
	v_max_f32_e64 v92, |v74|, |v75|
	v_max3_f32 v34, v34, v67, v90
	v_pk_mul_f32 v[70:71], v[20:21], v[70:71]
	v_pk_mul_f32 v[68:69], v[18:19], v[68:69]
	v_max_f32_e64 v93, |v84|, |v85|
	v_max_f32_e64 v94, |v86|, |v87|
	v_max3_f32 v34, v34, v91, v92
	v_pk_mul_f32 v[44:45], v[24:25], v[44:45]
	v_pk_mul_f32 v[42:43], v[22:23], v[42:43]
	v_max_f32_e64 v95, |v68|, |v69|
	v_max_f32_e64 v96, |v70|, |v71|
	v_max3_f32 v34, v34, v93, v94
	v_pk_mul_f32 v[40:41], v[28:29], v[40:41]
	v_pk_mul_f32 v[38:39], v[26:27], v[38:39]
	v_max_f32_e64 v97, |v42|, |v43|
	v_max_f32_e64 v98, |v44|, |v45|
	v_max3_f32 v34, v34, v95, v96
	v_pk_mul_f32 v[36:37], v[32:33], v[36:37]
	v_max_f32_e64 v99, |v38|, |v39|
	v_max_f32_e64 v100, |v40|, |v41|
	v_max3_f32 v34, v34, v97, v98
	v_max_f32_e64 v101, |v88|, |v89|
	v_max3_f32 v34, v34, v99, v100
	v_max_f32_e64 v35, |v36|, |v37|
	v_max3_f32 v34, v34, v101, v35
	s_nop 0
	s_waitcnt lgkmcnt(0)
	s_nop 0
	s_nop 1
	v_max_f32_dpp v34, v34, v34 quad_perm:[1,0,3,2] row_mask:0xf bank_mask:0xf bound_ctrl:1
	s_nop 0
	s_waitcnt lgkmcnt(0)
	s_nop 0
	s_nop 1
	v_max_f32_dpp v34, v34, v34 quad_perm:[2,3,0,1] row_mask:0xf bank_mask:0xf bound_ctrl:1
	s_nop 0
	s_waitcnt lgkmcnt(0)
	s_nop 0
	s_nop 1
	v_max_f32_dpp v34, v34, v34 row_half_mirror row_mask:0xf bank_mask:0xf bound_ctrl:1
	s_nop 0
	s_waitcnt lgkmcnt(0)
	s_nop 0
	s_nop 1
	v_max_f32_dpp v34, v34, v34 row_mirror row_mask:0xf bank_mask:0xf bound_ctrl:1
	s_nop 0
	s_waitcnt lgkmcnt(0)
	s_nop 0
	s_nop 1
	v_max_f32_dpp v34, v34, v34 row_bcast:15 row_mask:0xa bank_mask:0xf
	s_nop 0
	s_waitcnt lgkmcnt(0)
; __device__ __forceinline__ float wave_max(float v) {
; #pragma unroll
;     for (int o = 1; o < 64; o <<= 1) v = fmaxf(v, __shfl_xor(v, o));
;     return v;
; }
;     ...
;                 mx = fmaxf(wave_max(mx), 1e-30f); const float qs = 127.0f / mx;
; #pragma unroll
;                 for (int q = 0; q < 8; ++q) o4[64 * q] = pack_i8x4(v[q].x * qs, v[q].y * qs, v[q].z * qs, v[q].w * qs);
;                 if (lane == 0) ((float*)(ws + WS_ROWQ))[row] = mx * (1.0f / 127.0f); }
	s_nop 1
	v_max_f32_dpp v34, v34, v34 row_bcast:31 row_mask:0xc bank_mask:0xf
	s_nop 0
	v_readlane_b32 s98, v34, 63
	s_nop 1
	v_mov_b32_e32 v34, s98
	v_max_f32_e32 v34, s8, v34
	v_div_scale_f32 v35, s[2:3], v34, v34, s9
	v_rcp_f32_e32 v67, v35
	v_div_scale_f32 v90, vcc, s9, v34, s9
	v_fma_f32 v91, -v35, v67, 1.0
	v_fmac_f32_e32 v67, v91, v67
	v_mul_f32_e32 v91, v90, v67
	v_fma_f32 v92, -v35, v91, v90
	v_fmac_f32_e32 v91, v92, v67
	v_fma_f32 v35, -v35, v91, v90
	v_div_fmas_f32 v35, v35, v67, v91
	v_div_fixup_f32 v35, v35, v34, s9
	v_mul_f32_e32 v67, v76, v35
	v_mul_f32_e32 v76, v77, v35
	v_mul_f32_e32 v77, v78, v35
	v_mul_f32_e32 v78, v79, v35
	v_rndne_f32_e32 v76, v76
	v_mul_f32_e32 v79, v80, v35
	v_mul_f32_e32 v80, v81, v35
	v_rndne_f32_e32 v67, v67
	v_rndne_f32_e32 v78, v78
	v_rndne_f32_e32 v77, v77
	v_cvt_i32_f32_e32 v76, v76
	v_mul_f32_e32 v81, v82, v35
	v_mul_f32_e32 v82, v83, v35
	v_rndne_f32_e32 v80, v80
	v_cvt_i32_f32_e32 v67, v67
	v_cvt_i32_f32_e32 v78, v78
	v_cvt_i32_f32_sdwa v77, v77 dst_sel:WORD_1 dst_unused:UNUSED_PAD src0_sel:DWORD
	v_rndne_f32_e32 v79, v79
	v_rndne_f32_e32 v81, v81
	v_rndne_f32_e32 v82, v82
	v_cvt_i32_f32_e32 v80, v80
	v_cvt_i32_f32_e32 v79, v79
	v_cvt_i32_f32_sdwa v81, v81 dst_sel:WORD_1 dst_unused:UNUSED_PAD src0_sel:DWORD
	v_cvt_i32_f32_e32 v82, v82
	v_lshlrev_b32_e32 v76, 8, v76
	v_perm_b32 v67, v78, v67, s10
	v_and_b32_e32 v77, 0xff0000, v77
	v_and_b32_e32 v76, 0xff00, v76
	v_lshlrev_b32_e32 v78, 8, v80
	v_or3_b32 v67, v67, v76, v77
	v_and_b32_e32 v78, 0xff00, v78
	global_store_dword v[54:55], v67, off offset:-1024
	v_and_b32_e32 v67, 0xff0000, v81
	v_perm_b32 v76, v82, v79, s10
	v_or3_b32 v67, v76, v78, v67
	global_store_dword v[54:55], v67, off offset:-768
	v_mul_f32_e32 v67, v72, v35
	v_mul_f32_e32 v72, v73, v35
	v_mul_f32_e32 v73, v74, v35
	v_mul_f32_e32 v74, v75, v35
	v_rndne_f32_e32 v72, v72
	v_rndne_f32_e32 v67, v67
	v_cvt_i32_f32_e32 v72, v72
	v_rndne_f32_e32 v73, v73
	v_rndne_f32_e32 v74, v74
	v_cvt_i32_f32_e32 v67, v67
	v_cvt_i32_f32_sdwa v73, v73 dst_sel:WORD_1 dst_unused:UNUSED_PAD src0_sel:DWORD
	v_cvt_i32_f32_e32 v74, v74
	v_lshlrev_b32_e32 v72, 8, v72
	v_and_b32_e32 v72, 0xff00, v72
	v_and_b32_e32 v73, 0xff0000, v73
	v_perm_b32 v67, v74, v67, s10
	v_or3_b32 v67, v67, v72, v73
	v_mul_f32_e32 v72, v85, v35
	v_mul_f32_e32 v39, v39, v35
	global_store_dword v[54:55], v67, off offset:-512
	v_mul_f32_e32 v67, v84, v35
	v_mul_f32_e32 v73, v86, v35
	v_mul_f32_e32 v74, v87, v35
	v_rndne_f32_e32 v72, v72
	v_mul_f32_e32 v38, v38, v35
	v_mul_f32_e32 v40, v40, v35
	v_mul_f32_e32 v41, v41, v35
	v_rndne_f32_e32 v39, v39
	v_rndne_f32_e32 v67, v67
	v_cvt_i32_f32_e32 v72, v72
	v_rndne_f32_e32 v73, v73
	v_rndne_f32_e32 v74, v74
	v_rndne_f32_e32 v38, v38
	v_cvt_i32_f32_e32 v39, v39
	v_rndne_f32_e32 v40, v40
	v_rndne_f32_e32 v41, v41
	v_cvt_i32_f32_e32 v67, v67
	v_cvt_i32_f32_sdwa v73, v73 dst_sel:WORD_1 dst_unused:UNUSED_PAD src0_sel:DWORD
	v_cvt_i32_f32_e32 v74, v74
	v_cvt_i32_f32_e32 v38, v38
	v_cvt_i32_f32_sdwa v40, v40 dst_sel:WORD_1 dst_unused:UNUSED_PAD src0_sel:DWORD
	v_cvt_i32_f32_e32 v41, v41
	v_lshlrev_b32_e32 v72, 8, v72
	v_lshlrev_b32_e32 v39, 8, v39
	v_and_b32_e32 v72, 0xff00, v72
	v_and_b32_e32 v73, 0xff0000, v73
	v_perm_b32 v67, v74, v67, s10
	v_and_b32_e32 v39, 0xff00, v39
	v_and_b32_e32 v40, 0xff0000, v40
	v_perm_b32 v38, v41, v38, s10
	v_or3_b32 v67, v67, v72, v73
	v_or3_b32 v38, v38, v39, v40
	global_store_dword v[54:55], v67, off offset:-256
	v_mul_f32_e32 v67, v68, v35
	v_mul_f32_e32 v68, v69, v35
	v_mul_f32_e32 v43, v43, v35
	global_store_dword v[54:55], v38, off offset:512
	v_mul_f32_e32 v38, v88, v35
	v_mul_f32_e32 v39, v89, v35
	v_mul_f32_e32 v69, v70, v35
	v_mul_f32_e32 v70, v71, v35
	v_rndne_f32_e32 v68, v68
	v_mul_f32_e32 v42, v42, v35
	v_mul_f32_e32 v44, v44, v35
	v_mul_f32_e32 v45, v45, v35
	v_rndne_f32_e32 v43, v43
	v_mul_f32_e32 v36, v36, v35
	v_mul_f32_e32 v35, v37, v35
	v_rndne_f32_e32 v37, v38
	v_rndne_f32_e32 v38, v39
	v_rndne_f32_e32 v67, v67
	v_cvt_i32_f32_e32 v68, v68
	v_rndne_f32_e32 v69, v69
	v_rndne_f32_e32 v70, v70
	v_rndne_f32_e32 v42, v42
	v_cvt_i32_f32_e32 v43, v43
	v_rndne_f32_e32 v44, v44
	v_rndne_f32_e32 v45, v45
	v_cvt_i32_f32_e32 v38, v38
	v_rndne_f32_e32 v36, v36
	v_rndne_f32_e32 v35, v35
	v_cvt_i32_f32_e32 v67, v67
	v_cvt_i32_f32_sdwa v69, v69 dst_sel:WORD_1 dst_unused:UNUSED_PAD src0_sel:DWORD
	v_cvt_i32_f32_e32 v70, v70
	v_cvt_i32_f32_e32 v42, v42
	v_cvt_i32_f32_sdwa v44, v44 dst_sel:WORD_1 dst_unused:UNUSED_PAD src0_sel:DWORD
	v_cvt_i32_f32_e32 v45, v45
	v_cvt_i32_f32_e32 v37, v37
	v_cvt_i32_f32_sdwa v36, v36 dst_sel:WORD_1 dst_unused:UNUSED_PAD src0_sel:DWORD
	v_cvt_i32_f32_e32 v35, v35
	v_lshlrev_b32_e32 v68, 8, v68
	v_lshlrev_b32_e32 v43, 8, v43
	v_lshlrev_b32_e32 v38, 8, v38
	v_and_b32_e32 v68, 0xff00, v68
	v_and_b32_e32 v69, 0xff0000, v69
	v_perm_b32 v67, v70, v67, s10
	v_and_b32_e32 v43, 0xff00, v43
	v_and_b32_e32 v44, 0xff0000, v44
	v_perm_b32 v42, v45, v42, s10
	v_and_b32_e32 v38, 0xff00, v38
	v_and_b32_e32 v36, 0xff0000, v36
	v_perm_b32 v35, v35, v37, s10
	v_or3_b32 v67, v67, v68, v69
	v_or3_b32 v42, v42, v43, v44
	v_or3_b32 v35, v35, v38, v36
	global_store_dword v[54:55], v67, off
	global_store_dword v[54:55], v42, off offset:256
	global_store_dword v[54:55], v35, off offset:768
	s_and_saveexec_b64 s[2:3], s[0:1]
	s_cbranch_execz .LBB0_150
	v_mul_f32_e32 v34, 0x3c010204, v34
	global_store_dword v[58:59], v34, off
	s_branch .LBB0_150

; template <bool SB> __device__ __forceinline__ void load_row(const void* xin, size_t row, int lane, f32x4 (&v)[8]) {
;     if (SB) { typedef _Float16 h16x4_t __attribute__((ext_vector_type(4))); const h16x4_t* xr = (const h16x4_t*)((const bf16*)xin + row * DM) + lane;
; #pragma unroll
;         for (int q = 0; q < 8; ++q) { const h16x4_t w = xr[64 * q]; v[q] = (f32x4){(float)w[0], (float)w[1], (float)w[2], (float)w[3]}; } }
;     ...
;             f32x4 v[8]; float ss = 0.f; load_row<SB>(xin, (size_t)row, lane, v);
; #pragma unroll
;             for (int q = 0; q < 8; ++q) ss += (v[q].x * v[q].x + v[q].y * v[q].y) + (v[q].z * v[q].z + v[q].w * v[q].w);
;             const float rstd = 1.0f / sqrtf(wave_sum(ss) * (1.0f / DM) + NORM_EPS);
.LBB0_360:
	v_lshl_add_u64 v[46:47], v[40:41], 0, v[34:35]
	global_load_dwordx2 v[56:57], v[46:47], off
	global_load_dwordx2 v[58:59], v[46:47], off offset:1536
	global_load_dwordx2 v[60:61], v[46:47], off offset:3584
	global_load_dwordx2 v[62:63], v[46:47], off offset:512
	global_load_dwordx2 v[64:65], v[46:47], off offset:1024
	global_load_dwordx2 v[66:67], v[46:47], off offset:2048
	global_load_dwordx2 v[68:69], v[46:47], off offset:2560
	global_load_dwordx2 v[70:71], v[46:47], off offset:3072
	v_add_u32_e32 v37, v37, v36
	v_cmp_gt_i32_e64 s[0:1], s7, v37
	v_lshl_add_u64 v[44:45], v[42:43], 0, v[34:35]
	v_lshl_add_u64 v[40:41], v[40:41], 0, v[38:39]
	v_lshl_add_u64 v[42:43], v[42:43], 0, v[38:39]
	s_waitcnt vmcnt(0)
	v_cvt_f32_f16_e32 v46, v56
	v_cvt_f32_f16_sdwa v47, v56 dst_sel:DWORD dst_unused:UNUSED_PAD src0_sel:WORD_1
	v_cvt_f32_f16_e32 v56, v57
	v_cvt_f32_f16_sdwa v57, v57 dst_sel:DWORD dst_unused:UNUSED_PAD src0_sel:WORD_1
	v_cvt_f32_f16_e32 v77, v63
	v_cvt_f32_f16_e32 v76, v62
	v_cvt_f32_f16_sdwa v63, v63 dst_sel:DWORD dst_unused:UNUSED_PAD src0_sel:WORD_1
	v_cvt_f32_f16_sdwa v62, v62 dst_sel:DWORD dst_unused:UNUSED_PAD src0_sel:WORD_1
	v_cvt_f32_f16_e32 v78, v64
	v_cvt_f32_f16_sdwa v79, v64 dst_sel:DWORD dst_unused:UNUSED_PAD src0_sel:WORD_1
	v_cvt_f32_f16_e32 v64, v65
	v_cvt_f32_f16_sdwa v65, v65 dst_sel:DWORD dst_unused:UNUSED_PAD src0_sel:WORD_1
	v_cvt_f32_f16_e32 v72, v58
	v_cvt_f32_f16_sdwa v73, v58 dst_sel:DWORD dst_unused:UNUSED_PAD src0_sel:WORD_1
	v_cvt_f32_f16_e32 v58, v59
	v_cvt_f32_f16_sdwa v59, v59 dst_sel:DWORD dst_unused:UNUSED_PAD src0_sel:WORD_1
	v_cvt_f32_f16_e32 v81, v67
	v_cvt_f32_f16_e32 v80, v66
	v_cvt_f32_f16_sdwa v67, v67 dst_sel:DWORD dst_unused:UNUSED_PAD src0_sel:WORD_1
	v_cvt_f32_f16_sdwa v66, v66 dst_sel:DWORD dst_unused:UNUSED_PAD src0_sel:WORD_1
	v_mul_f32_e32 v86, v47, v47
	v_mul_f32_e32 v88, v57, v57
	v_pk_mul_f32 v[90:91], v[62:63], v[62:63]
	v_cvt_f32_f16_e32 v83, v69
	v_cvt_f32_f16_e32 v82, v68
	v_cvt_f32_f16_sdwa v69, v69 dst_sel:DWORD dst_unused:UNUSED_PAD src0_sel:WORD_1
	v_cvt_f32_f16_sdwa v68, v68 dst_sel:DWORD dst_unused:UNUSED_PAD src0_sel:WORD_1
	v_mul_f32_e32 v92, v79, v79
	v_mul_f32_e32 v94, v65, v65
	v_mov_b32_e32 v112, v76
	v_mov_b32_e32 v113, v62
	v_mov_b32_e32 v62, v77
	v_pk_fma_f32 v[86:87], v[46:47], v[46:47], v[86:87] op_sel_hi:[1,1,0]
	v_pk_fma_f32 v[88:89], v[56:57], v[56:57], v[88:89] op_sel_hi:[1,1,0]
	v_pk_fma_f32 v[76:77], v[76:77], v[76:77], v[90:91]
	v_cvt_f32_f16_e32 v84, v70
	v_cvt_f32_f16_sdwa v85, v70 dst_sel:DWORD dst_unused:UNUSED_PAD src0_sel:WORD_1
	v_cvt_f32_f16_e32 v70, v71
	v_cvt_f32_f16_sdwa v71, v71 dst_sel:DWORD dst_unused:UNUSED_PAD src0_sel:WORD_1
	v_pk_mul_f32 v[96:97], v[72:73], v[72:73]
	v_pk_mul_f32 v[98:99], v[58:59], v[58:59]
	v_pk_fma_f32 v[90:91], v[78:79], v[78:79], v[92:93] op_sel_hi:[1,1,0]
	v_pk_fma_f32 v[92:93], v[64:65], v[64:65], v[94:95] op_sel_hi:[1,1,0]
	v_pk_add_f32 v[76:77], v[76:77], v[76:77] op_sel:[0,1] op_sel_hi:[1,0]
	v_pk_add_f32 v[86:87], v[86:87], v[88:89]
	v_cvt_f32_f16_e32 v74, v60
	v_cvt_f32_f16_sdwa v75, v60 dst_sel:DWORD dst_unused:UNUSED_PAD src0_sel:WORD_1
	v_cvt_f32_f16_e32 v60, v61
	v_cvt_f32_f16_sdwa v61, v61 dst_sel:DWORD dst_unused:UNUSED_PAD src0_sel:WORD_1
	v_mov_b32_e32 v91, v98
	v_mov_b32_e32 v93, v99
	v_mov_b32_e32 v87, v96
	v_mov_b32_e32 v77, v97
	v_pk_mul_f32 v[100:101], v[66:67], v[66:67]
	v_pk_add_f32 v[88:89], v[90:91], v[92:93]
	v_pk_add_f32 v[76:77], v[86:87], v[76:77]
	v_pk_mul_f32 v[102:103], v[68:69], v[68:69]
	v_mov_b32_e32 v114, v80
	v_mov_b32_e32 v115, v66
	v_mov_b32_e32 v66, v81
	v_pk_fma_f32 v[80:81], v[80:81], v[80:81], v[100:101]
	v_pk_add_f32 v[76:77], v[76:77], v[88:89]
	v_mul_f32_e32 v104, v85, v85
	v_mul_f32_e32 v106, v71, v71
	v_mov_b32_e32 v116, v82
	v_mov_b32_e32 v117, v68
	v_mov_b32_e32 v68, v83
	v_pk_fma_f32 v[82:83], v[82:83], v[82:83], v[102:103]
	v_pk_add_f32 v[80:81], v[80:81], v[80:81] op_sel:[0,1] op_sel_hi:[1,0]
	v_pk_add_f32 v[76:77], v[76:77], v[76:77] op_sel:[0,1] op_sel_hi:[1,0]
	v_pk_mul_f32 v[108:109], v[74:75], v[74:75]
	v_pk_mul_f32 v[110:111], v[60:61], v[60:61]
	v_pk_fma_f32 v[94:95], v[84:85], v[84:85], v[104:105] op_sel_hi:[1,1,0]
	v_pk_fma_f32 v[100:101], v[70:71], v[70:71], v[106:107] op_sel_hi:[1,1,0]
	v_pk_add_f32 v[82:83], v[82:83], v[82:83] op_sel:[0,1] op_sel_hi:[1,0]
	v_pk_add_f32 v[76:77], v[76:77], v[80:81]
	v_mov_b32_e32 v95, v110
	v_mov_b32_e32 v101, v111
	v_mov_b32_e32 v83, v109
	v_mov_b32_e32 v77, v108
	v_pk_add_f32 v[90:91], v[94:95], v[100:101]
	v_pk_add_f32 v[76:77], v[76:77], v[82:83]
	s_nop 0
	v_pk_add_f32 v[76:77], v[76:77], v[90:91]
	s_nop 0
	v_add_f32_e32 v55, v76, v77
	s_nop 0
	s_waitcnt lgkmcnt(0)
; __device__ __forceinline__ unsigned pk2(float lo, float hi) { return pg8::cvt_pk_bf16(lo, hi); }
; __device__ __forceinline__ float wave_sum(float v) {
; #pragma unroll
;     for (int o = 1; o < 64; o <<= 1) v += __shfl_xor(v, o);
;     return v;
; }
;     ...
;             const float rstd = 1.0f / sqrtf(wave_sum(ss) * (1.0f / DM) + NORM_EPS);
;             if (F8 == 2) { unsigned* o4 = (unsigned*)((unsigned char*)xn + (size_t)row * DM) + lane; float mx = 0.f;
; #pragma unroll
;                 for (int q = 0; q < 8; ++q) { v[q] = v[q] * rstd * gn[q]; mx = fmaxf(fmaxf(mx, fmaxf(fabsf(v[q].x), fabsf(v[q].y))), fmaxf(fabsf(v[q].z), fabsf(v[q].w))); }
;                 mx = fmaxf(wave_max(mx), 1e-30f); const float qs = 127.0f / mx;
; #pragma unroll
;                 for (int q = 0; q < 8; ++q) o4[64 * q] = pack_i8x4(v[q].x * qs, v[q].y * qs, v[q].z * qs, v[q].w * qs);
;                 if (lane == 0) ((float*)(ws + WS_ROWQ))[row] = mx * (1.0f / 127.0f); }
;             else if (F8 == 1) { unsigned* o4 = (unsigned*)((unsigned char*)xn + (size_t)row * DM) + lane;
; #pragma unroll
;                 for (int q = 0; q < 8; ++q) { const f32x4 y = v[q] * (rstd * pg8::X8_SCALE) * gn[q]; unsigned w = 0u;
;                     w = __builtin_amdgcn_cvt_pk_fp8_f32(__builtin_amdgcn_fmed3f(y.x, -448.f, 448.f), __builtin_amdgcn_fmed3f(y.y, -448.f, 448.f), w, false);
;                     w = __builtin_amdgcn_cvt_pk_fp8_f32(__builtin_amdgcn_fmed3f(y.z, -448.f, 448.f), __builtin_amdgcn_fmed3f(y.w, -448.f, 448.f), w, true); o4[64 * q] = w; } }
;             else { v2u* o8 = (v2u*)(xn + (size_t)row * DM) + lane;
; #pragma unroll
;                 for (int q = 0; q < 8; ++q) { const f32x4 y = v[q] * rstd * gn[q]; v2u w; w.x = pk2(y.x, y.y); w.y = pk2(y.z, y.w); o8[64 * q] = w; } }
	s_nop 1
	v_add_f32_dpp v55, v55, v55 quad_perm:[1,0,3,2] row_mask:0xf bank_mask:0xf bound_ctrl:1
	s_nop 0
	s_waitcnt lgkmcnt(0)
	s_nop 1
	v_add_f32_dpp v55, v55, v55 quad_perm:[2,3,0,1] row_mask:0xf bank_mask:0xf bound_ctrl:1
	s_nop 0
	s_waitcnt lgkmcnt(0)
	s_nop 1
	v_add_f32_dpp v55, v55, v55 row_half_mirror row_mask:0xf bank_mask:0xf bound_ctrl:1
	s_nop 0
	s_waitcnt lgkmcnt(0)
	s_nop 1
	v_add_f32_dpp v55, v55, v55 row_mirror row_mask:0xf bank_mask:0xf bound_ctrl:1
	s_nop 0
	s_waitcnt lgkmcnt(0)
	s_nop 1
	v_add_f32_dpp v55, v55, v55 row_bcast:15 row_mask:0xa bank_mask:0xf
	s_nop 0
	s_waitcnt lgkmcnt(0)
	s_nop 1
	v_add_f32_dpp v55, v55, v55 row_bcast:31 row_mask:0xc bank_mask:0xf
	s_nop 0
	v_readlane_b32 s98, v55, 63
	s_nop 1
	v_mov_b32_e32 v55, s98
	v_fmamk_f32 v55, v55, 0x3a000000, v53
	v_mul_f32_e32 v76, 0x4f800000, v55
	v_cmp_gt_f32_e32 vcc, s6, v55
	s_nop 1
	v_cndmask_b32_e32 v55, v55, v76, vcc
	v_sqrt_f32_e32 v76, v55
	s_nop 0
	v_add_u32_e32 v77, -1, v76
	v_add_u32_e32 v80, 1, v76
	v_fma_f32 v81, -v77, v76, v55
	v_fma_f32 v82, -v80, v76, v55
	v_cmp_ge_f32_e64 s[2:3], 0, v81
	s_nop 1
	v_cndmask_b32_e64 v76, v76, v77, s[2:3]
	v_cmp_lt_f32_e64 s[2:3], 0, v82
	s_nop 1
	v_cndmask_b32_e64 v76, v76, v80, s[2:3]
	v_mul_f32_e32 v77, 0x37800000, v76
	v_cndmask_b32_e32 v76, v76, v77, vcc
	v_cmp_class_f32_e32 vcc, v55, v54
	s_nop 1
	v_cndmask_b32_e32 v55, v76, v55, vcc
	v_div_scale_f32 v76, s[2:3], v55, v55, 1.0
	v_rcp_f32_e32 v80, v76
	v_div_scale_f32 v77, vcc, 1.0, v55, 1.0
	v_fma_f32 v81, -v76, v80, 1.0
	v_fmac_f32_e32 v80, v81, v80
	v_mul_f32_e32 v81, v77, v80
	v_fma_f32 v82, -v76, v81, v77
	v_fmac_f32_e32 v81, v82, v80
	v_fma_f32 v76, -v76, v81, v77
	v_div_fmas_f32 v76, v76, v80, v81
	v_div_fixup_f32 v76, v76, v55, 1.0
	v_pk_mul_f32 v[46:47], v[46:47], v[76:77] op_sel_hi:[1,0]
	v_pk_mul_f32 v[56:57], v[56:57], v[76:77] op_sel_hi:[1,0]
	v_pk_mul_f32 v[80:81], v[112:113], v[76:77] op_sel_hi:[1,0]
	v_pk_mul_f32 v[62:63], v[62:63], v[76:77] op_sel_hi:[1,0]
	v_pk_mul_f32 v[78:79], v[78:79], v[76:77] op_sel_hi:[1,0]
	v_pk_mul_f32 v[64:65], v[64:65], v[76:77] op_sel_hi:[1,0]
	v_pk_mul_f32 v[72:73], v[72:73], v[76:77] op_sel_hi:[1,0]
	v_pk_mul_f32 v[58:59], v[58:59], v[76:77] op_sel_hi:[1,0]
	v_pk_mul_f32 v[82:83], v[114:115], v[76:77] op_sel_hi:[1,0]
	v_pk_mul_f32 v[66:67], v[66:67], v[76:77] op_sel_hi:[1,0]
	v_pk_mul_f32 v[86:87], v[116:117], v[76:77] op_sel_hi:[1,0]
	v_pk_mul_f32 v[68:69], v[68:69], v[76:77] op_sel_hi:[1,0]
	v_pk_mul_f32 v[84:85], v[84:85], v[76:77] op_sel_hi:[1,0]
	v_pk_mul_f32 v[70:71], v[70:71], v[76:77] op_sel_hi:[1,0]
	v_pk_mul_f32 v[74:75], v[74:75], v[76:77] op_sel_hi:[1,0]
	v_pk_mul_f32 v[60:61], v[60:61], v[76:77] op_sel_hi:[1,0]
	v_pk_mul_f32 v[56:57], v[4:5], v[56:57]
	v_pk_mul_f32 v[46:47], v[2:3], v[46:47]
	s_and_b64 vcc, exec, s[0:1]
	v_pk_mul_f32 v[62:63], v[8:9], v[62:63]
	v_pk_mul_f32 v[76:77], v[6:7], v[80:81]
	v_pk_mul_f32 v[64:65], v[12:13], v[64:65]
	v_pk_mul_f32 v[78:79], v[10:11], v[78:79]
	v_pk_mul_f32 v[58:59], v[16:17], v[58:59]
	v_pk_mul_f32 v[72:73], v[14:15], v[72:73]
	v_pk_mul_f32 v[66:67], v[20:21], v[66:67]
	v_pk_mul_f32 v[80:81], v[18:19], v[82:83]
	v_pk_mul_f32 v[68:69], v[24:25], v[68:69]
	v_pk_mul_f32 v[82:83], v[22:23], v[86:87]
	v_pk_mul_f32 v[70:71], v[28:29], v[70:71]
	v_pk_mul_f32 v[84:85], v[26:27], v[84:85]
	v_pk_mul_f32 v[60:61], v[32:33], v[60:61]
	v_pk_mul_f32 v[74:75], v[30:31], v[74:75]
	v_cvt_pk_bf16_f32 v46, v46, v47
	v_cvt_pk_bf16_f32 v47, v56, v57
	v_cvt_pk_bf16_f32 v56, v76, v77
	v_cvt_pk_bf16_f32 v57, v62, v63
	v_cvt_pk_bf16_f32 v62, v78, v79
	v_cvt_pk_bf16_f32 v63, v64, v65
	v_cvt_pk_bf16_f32 v64, v72, v73
	v_cvt_pk_bf16_f32 v65, v58, v59
	v_cvt_pk_bf16_f32 v58, v80, v81
	v_cvt_pk_bf16_f32 v59, v66, v67
	v_cvt_pk_bf16_f32 v66, v82, v83
	v_cvt_pk_bf16_f32 v67, v68, v69
	v_cvt_pk_bf16_f32 v68, v84, v85
	v_cvt_pk_bf16_f32 v69, v70, v71
	v_cvt_pk_bf16_f32 v70, v74, v75
	v_cvt_pk_bf16_f32 v71, v60, v61
	global_store_dwordx2 v[44:45], v[46:47], off offset:-2048
	global_store_dwordx2 v[44:45], v[56:57], off offset:-1536
	global_store_dwordx2 v[44:45], v[62:63], off offset:-1024
	global_store_dwordx2 v[44:45], v[64:65], off offset:-512
	global_store_dwordx2 v[44:45], v[58:59], off
	global_store_dwordx2 v[44:45], v[66:67], off offset:512
	global_store_dwordx2 v[44:45], v[68:69], off offset:1024
	global_store_dwordx2 v[44:45], v[70:71], off offset:1536
	s_cbranch_vccnz .LBB0_360

; template <bool SB> __device__ __forceinline__ void load_row(const void* xin, size_t row, int lane, f32x4 (&v)[8]) {
;     if (SB) { typedef _Float16 h16x4_t __attribute__((ext_vector_type(4))); const h16x4_t* xr = (const h16x4_t*)((const bf16*)xin + row * DM) + lane;
; #pragma unroll
;         for (int q = 0; q < 8; ++q) { const h16x4_t w = xr[64 * q]; v[q] = (f32x4){(float)w[0], (float)w[1], (float)w[2], (float)w[3]}; } }
;     ...
;             f32x4 v[8]; float ss = 0.f; load_row<SB>(xin, (size_t)row, lane, v);
; #pragma unroll
;             for (int q = 0; q < 8; ++q) ss += (v[q].x * v[q].x + v[q].y * v[q].y) + (v[q].z * v[q].z + v[q].w * v[q].w);
;             const float rstd = 1.0f / sqrtf(wave_sum(ss) * (1.0f / DM) + NORM_EPS);
.LBB0_770:
	global_load_dwordx2 v[56:57], v[38:39], off offset:-3584
	global_load_dwordx2 v[58:59], v[38:39], off offset:-3072
	global_load_dwordx2 v[60:61], v[38:39], off offset:-2560
	global_load_dwordx2 v[62:63], v[38:39], off offset:-2048
	global_load_dwordx2 v[64:65], v[38:39], off offset:-1536
	global_load_dwordx2 v[66:67], v[38:39], off offset:-1024
	global_load_dwordx2 v[68:69], v[38:39], off offset:-512
	global_load_dwordx2 v[70:71], v[38:39], off
	s_waitcnt vmcnt(7)
	v_cvt_f32_f16_sdwa v73, v56 dst_sel:DWORD dst_unused:UNUSED_PAD src0_sel:WORD_1
	v_cvt_f32_f16_sdwa v75, v57 dst_sel:DWORD dst_unused:UNUSED_PAD src0_sel:WORD_1
	v_cvt_f32_f16_e32 v74, v57
	s_waitcnt vmcnt(6)
	v_cvt_f32_f16_sdwa v57, v58 dst_sel:DWORD dst_unused:UNUSED_PAD src0_sel:WORD_1
	v_cvt_f32_f16_sdwa v77, v59 dst_sel:DWORD dst_unused:UNUSED_PAD src0_sel:WORD_1
	v_cvt_f32_f16_e32 v72, v56
	v_cvt_f32_f16_e32 v56, v58
	v_cvt_f32_f16_e32 v76, v59
	s_waitcnt vmcnt(5)
	v_cvt_f32_f16_sdwa v59, v60 dst_sel:DWORD dst_unused:UNUSED_PAD src0_sel:WORD_1
	v_cvt_f32_f16_sdwa v79, v61 dst_sel:DWORD dst_unused:UNUSED_PAD src0_sel:WORD_1
	v_cvt_f32_f16_e32 v58, v60
	v_cvt_f32_f16_e32 v78, v61
	s_waitcnt vmcnt(4)
	v_cvt_f32_f16_sdwa v61, v62 dst_sel:DWORD dst_unused:UNUSED_PAD src0_sel:WORD_1
	v_cvt_f32_f16_sdwa v81, v63 dst_sel:DWORD dst_unused:UNUSED_PAD src0_sel:WORD_1
	v_cvt_f32_f16_e32 v60, v62
	v_cvt_f32_f16_e32 v80, v63
	s_waitcnt vmcnt(3)
	v_cvt_f32_f16_sdwa v63, v64 dst_sel:DWORD dst_unused:UNUSED_PAD src0_sel:WORD_1
	v_cvt_f32_f16_e32 v62, v64
	v_cvt_f32_f16_sdwa v83, v65 dst_sel:DWORD dst_unused:UNUSED_PAD src0_sel:WORD_1
	v_cvt_f32_f16_e32 v82, v65
	v_mov_b32_e32 v90, v73
	v_mov_b32_e32 v91, v57
	v_mov_b32_e32 v94, v75
	v_mov_b32_e32 v95, v77
	s_waitcnt vmcnt(2)
	v_cvt_f32_f16_sdwa v65, v66 dst_sel:DWORD dst_unused:UNUSED_PAD src0_sel:WORD_1
	v_cvt_f32_f16_e32 v64, v66
	v_cvt_f32_f16_sdwa v85, v67 dst_sel:DWORD dst_unused:UNUSED_PAD src0_sel:WORD_1
	v_cvt_f32_f16_e32 v84, v67
	s_waitcnt vmcnt(1)
	v_cvt_f32_f16_sdwa v67, v68 dst_sel:DWORD dst_unused:UNUSED_PAD src0_sel:WORD_1
	v_cvt_f32_f16_e32 v66, v68
	v_cvt_f32_f16_sdwa v87, v69 dst_sel:DWORD dst_unused:UNUSED_PAD src0_sel:WORD_1
	v_cvt_f32_f16_e32 v86, v69
	s_waitcnt vmcnt(0)
	v_cvt_f32_f16_sdwa v69, v70 dst_sel:DWORD dst_unused:UNUSED_PAD src0_sel:WORD_1
	v_cvt_f32_f16_e32 v68, v70
	v_cvt_f32_f16_sdwa v89, v71 dst_sel:DWORD dst_unused:UNUSED_PAD src0_sel:WORD_1
	v_cvt_f32_f16_e32 v88, v71
	v_mov_b32_e32 v70, v72
	v_mov_b32_e32 v71, v56
	v_mov_b32_e32 v92, v74
	v_mov_b32_e32 v93, v76
	v_mov_b32_e32 v98, v59
	v_mov_b32_e32 v99, v79
	v_pk_mul_f32 v[90:91], v[90:91], v[90:91]
	v_pk_mul_f32 v[94:95], v[94:95], v[94:95]
	v_mov_b32_e32 v96, v58
	v_mov_b32_e32 v97, v78
	v_pk_mul_f32 v[98:99], v[98:99], v[98:99]
	v_pk_fma_f32 v[70:71], v[70:71], v[70:71], v[90:91]
	v_pk_fma_f32 v[90:91], v[92:93], v[92:93], v[94:95]
	v_mul_f32_e32 v100, v61, v61
	v_mul_f32_e32 v102, v81, v81
	v_pk_fma_f32 v[92:93], v[96:97], v[96:97], v[98:99]
	v_pk_add_f32 v[70:71], v[70:71], v[90:91]
	v_pk_mul_f32 v[104:105], v[62:63], v[62:63]
	v_pk_mul_f32 v[106:107], v[82:83], v[82:83]
	v_pk_fma_f32 v[100:101], v[60:61], v[60:61], v[100:101] op_sel_hi:[1,1,0]
	v_pk_fma_f32 v[102:103], v[80:81], v[80:81], v[102:103] op_sel_hi:[1,1,0]
	v_pk_add_f32 v[90:91], v[92:93], v[92:93] op_sel:[0,1] op_sel_hi:[1,0]
	v_pk_add_f32 v[70:71], v[70:71], v[70:71] op_sel:[0,1] op_sel_hi:[1,0]
	v_mov_b32_e32 v110, v65
	v_mov_b32_e32 v111, v85
	v_mov_b32_e32 v101, v106
	v_mov_b32_e32 v103, v107
	v_mov_b32_e32 v91, v105
	v_mov_b32_e32 v71, v104
	v_mov_b32_e32 v108, v64
	v_mov_b32_e32 v109, v84
	v_pk_mul_f32 v[110:111], v[110:111], v[110:111]
	v_pk_add_f32 v[92:93], v[100:101], v[102:103]
	v_pk_add_f32 v[70:71], v[70:71], v[90:91]
	v_mul_f32_e32 v112, v67, v67
	v_mul_f32_e32 v114, v87, v87
	v_pk_fma_f32 v[94:95], v[108:109], v[108:109], v[110:111]
	v_pk_add_f32 v[70:71], v[70:71], v[92:93]
	v_pk_mul_f32 v[116:117], v[68:69], v[68:69]
	v_pk_mul_f32 v[118:119], v[88:89], v[88:89]
	v_pk_fma_f32 v[112:113], v[66:67], v[66:67], v[112:113] op_sel_hi:[1,1,0]
	v_pk_fma_f32 v[114:115], v[86:87], v[86:87], v[114:115] op_sel_hi:[1,1,0]
	v_pk_add_f32 v[94:95], v[94:95], v[94:95] op_sel:[0,1] op_sel_hi:[1,0]
	v_pk_add_f32 v[70:71], v[70:71], v[70:71] op_sel:[0,1] op_sel_hi:[1,0]
	v_mov_b32_e32 v113, v118
	v_mov_b32_e32 v115, v119
	v_mov_b32_e32 v95, v117
	v_mov_b32_e32 v71, v116
	v_pk_add_f32 v[96:97], v[112:113], v[114:115]
	v_pk_add_f32 v[70:71], v[70:71], v[94:95]
	s_nop 0
	v_pk_add_f32 v[70:71], v[70:71], v[96:97]
	s_nop 0
	v_add_f32_e32 v55, v70, v71
	s_nop 0
	s_waitcnt lgkmcnt(0)
	s_nop 1
	v_add_f32_dpp v55, v55, v55 quad_perm:[1,0,3,2] row_mask:0xf bank_mask:0xf bound_ctrl:1
	s_nop 0
	s_waitcnt lgkmcnt(0)
	s_nop 1
	v_add_f32_dpp v55, v55, v55 quad_perm:[2,3,0,1] row_mask:0xf bank_mask:0xf bound_ctrl:1
	s_nop 0
	s_waitcnt lgkmcnt(0)
	s_nop 1
	v_add_f32_dpp v55, v55, v55 row_half_mirror row_mask:0xf bank_mask:0xf bound_ctrl:1
	s_nop 0
	s_waitcnt lgkmcnt(0)
	s_nop 1
	v_add_f32_dpp v55, v55, v55 row_mirror row_mask:0xf bank_mask:0xf bound_ctrl:1
	s_nop 0
	s_waitcnt lgkmcnt(0)
	s_nop 1
	v_add_f32_dpp v55, v55, v55 row_bcast:15 row_mask:0xa bank_mask:0xf
	s_nop 0
	s_waitcnt lgkmcnt(0)
; __device__ __forceinline__ float wave_max(float v) {
; #pragma unroll
;     for (int o = 1; o < 64; o <<= 1) v = fmaxf(v, __shfl_xor(v, o));
;     return v;
; }
;     ...
;             const float rstd = 1.0f / sqrtf(wave_sum(ss) * (1.0f / DM) + NORM_EPS);
;             if (F8 == 2) { unsigned* o4 = (unsigned*)((unsigned char*)xn + (size_t)row * DM) + lane; float mx = 0.f;
; #pragma unroll
;                 for (int q = 0; q < 8; ++q) { v[q] = v[q] * rstd * gn[q]; mx = fmaxf(fmaxf(mx, fmaxf(fabsf(v[q].x), fabsf(v[q].y))), fmaxf(fabsf(v[q].z), fabsf(v[q].w))); }
;                 mx = fmaxf(wave_max(mx), 1e-30f); const float qs = 127.0f / mx;
	s_nop 1
	v_add_f32_dpp v55, v55, v55 row_bcast:31 row_mask:0xc bank_mask:0xf
	s_nop 0
	v_readlane_b32 s98, v55, 63
	s_nop 1
	v_mov_b32_e32 v55, s98
	v_fmamk_f32 v55, v55, 0x3a000000, v53
	v_mul_f32_e32 v70, 0x4f800000, v55
	v_cmp_gt_f32_e32 vcc, s4, v55
	s_nop 1
	v_cndmask_b32_e32 v55, v55, v70, vcc
	v_sqrt_f32_e32 v70, v55
	s_nop 0
	v_add_u32_e32 v71, -1, v70
	v_add_u32_e32 v90, 1, v70
	v_fma_f32 v91, -v71, v70, v55
	v_fma_f32 v92, -v90, v70, v55
	v_cmp_ge_f32_e64 s[2:3], 0, v91
	s_nop 1
	v_cndmask_b32_e64 v70, v70, v71, s[2:3]
	v_cmp_lt_f32_e64 s[2:3], 0, v92
	s_nop 1
	v_cndmask_b32_e64 v70, v70, v90, s[2:3]
	v_mul_f32_e32 v71, 0x37800000, v70
	v_cndmask_b32_e32 v70, v70, v71, vcc
	v_cmp_class_f32_e32 vcc, v55, v54
	s_nop 1
	v_cndmask_b32_e32 v55, v70, v55, vcc
	v_div_scale_f32 v70, s[2:3], v55, v55, 1.0
	v_rcp_f32_e32 v71, v70
	v_div_scale_f32 v90, vcc, 1.0, v55, 1.0
	v_fma_f32 v91, -v70, v71, 1.0
	v_fmac_f32_e32 v71, v91, v71
	v_mul_f32_e32 v91, v90, v71
	v_fma_f32 v92, -v70, v91, v90
	v_fmac_f32_e32 v91, v92, v71
	v_fma_f32 v70, -v70, v91, v90
	v_div_fmas_f32 v70, v70, v71, v91
	v_div_fixup_f32 v70, v70, v55, 1.0
	v_pk_mul_f32 v[74:75], v[74:75], v[70:71] op_sel_hi:[1,0]
	v_pk_mul_f32 v[72:73], v[72:73], v[70:71] op_sel_hi:[1,0]
	v_pk_mul_f32 v[74:75], v[4:5], v[74:75]
	v_pk_mul_f32 v[56:57], v[56:57], v[70:71] op_sel_hi:[1,0]
	v_pk_mul_f32 v[76:77], v[76:77], v[70:71] op_sel_hi:[1,0]
	v_pk_mul_f32 v[58:59], v[58:59], v[70:71] op_sel_hi:[1,0]
	v_pk_mul_f32 v[78:79], v[78:79], v[70:71] op_sel_hi:[1,0]
	v_pk_mul_f32 v[60:61], v[60:61], v[70:71] op_sel_hi:[1,0]
	v_pk_mul_f32 v[80:81], v[80:81], v[70:71] op_sel_hi:[1,0]
	v_pk_mul_f32 v[72:73], v[2:3], v[72:73]
	v_max_f32_e64 v71, |v74|, |v75|
	v_pk_mul_f32 v[76:77], v[8:9], v[76:77]
	v_pk_mul_f32 v[56:57], v[6:7], v[56:57]
	v_max_f32_e64 v55, |v72|, |v73|
	v_pk_mul_f32 v[62:63], v[62:63], v[70:71] op_sel_hi:[1,0]
	v_pk_mul_f32 v[78:79], v[12:13], v[78:79]
	v_pk_mul_f32 v[58:59], v[10:11], v[58:59]
	v_max_f32_e64 v90, |v56|, |v57|
	v_max_f32_e64 v91, |v76|, |v77|
	v_max3_f32 v55, v55, 0, v71
	v_pk_mul_f32 v[62:63], v[18:19], v[62:63]
	v_pk_mul_f32 v[80:81], v[16:17], v[80:81]
	v_pk_mul_f32 v[60:61], v[14:15], v[60:61]
	v_max_f32_e64 v92, |v58|, |v59|
	v_max_f32_e64 v93, |v78|, |v79|
	v_max3_f32 v55, v55, v90, v91
	v_pk_mul_f32 v[82:83], v[82:83], v[70:71] op_sel_hi:[1,0]
	v_max_f32_e64 v71, |v62|, |v63|
	v_max_f32_e64 v94, |v60|, |v61|
	v_max_f32_e64 v95, |v80|, |v81|
	v_max3_f32 v55, v55, v92, v93
	v_pk_mul_f32 v[82:83], v[20:21], v[82:83]
	v_pk_mul_f32 v[64:65], v[64:65], v[70:71] op_sel_hi:[1,0]
	v_max3_f32 v55, v55, v94, v95
	v_max_f32_e64 v90, |v82|, |v83|
	v_pk_mul_f32 v[64:65], v[22:23], v[64:65]
	v_max3_f32 v55, v55, v71, v90
	v_pk_mul_f32 v[84:85], v[84:85], v[70:71] op_sel_hi:[1,0]
	v_max_f32_e64 v71, |v64|, |v65|
	v_pk_mul_f32 v[84:85], v[24:25], v[84:85]
	v_pk_mul_f32 v[66:67], v[66:67], v[70:71] op_sel_hi:[1,0]
	v_pk_mul_f32 v[86:87], v[86:87], v[70:71] op_sel_hi:[1,0]
	v_max_f32_e64 v90, |v84|, |v85|
	v_pk_mul_f32 v[86:87], v[28:29], v[86:87]
	v_pk_mul_f32 v[66:67], v[26:27], v[66:67]
	v_max3_f32 v55, v55, v71, v90
	v_max_f32_e64 v71, |v66|, |v67|
	v_max_f32_e64 v90, |v86|, |v87|
	v_max3_f32 v55, v55, v71, v90
	v_pk_mul_f32 v[68:69], v[68:69], v[70:71] op_sel_hi:[1,0]
	v_pk_mul_f32 v[70:71], v[88:89], v[70:71] op_sel_hi:[1,0]
	v_pk_mul_f32 v[68:69], v[30:31], v[68:69]
	v_pk_mul_f32 v[70:71], v[32:33], v[70:71]
	v_max_f32_e64 v88, |v68|, |v69|
	v_max_f32_e64 v89, |v70|, |v71|
	v_max3_f32 v55, v55, v88, v89
	s_nop 0
	s_waitcnt lgkmcnt(0)
	s_nop 0
	s_nop 1
	v_max_f32_dpp v55, v55, v55 quad_perm:[1,0,3,2] row_mask:0xf bank_mask:0xf bound_ctrl:1
	s_nop 0
	s_waitcnt lgkmcnt(0)
	s_nop 0
	s_nop 1
	v_max_f32_dpp v55, v55, v55 quad_perm:[2,3,0,1] row_mask:0xf bank_mask:0xf bound_ctrl:1
	s_nop 0
	s_waitcnt lgkmcnt(0)
	s_nop 0
	s_nop 1
	v_max_f32_dpp v55, v55, v55 row_half_mirror row_mask:0xf bank_mask:0xf bound_ctrl:1
	s_nop 0
	s_waitcnt lgkmcnt(0)
	s_nop 0
	s_nop 1
	v_max_f32_dpp v55, v55, v55 row_mirror row_mask:0xf bank_mask:0xf bound_ctrl:1
	s_nop 0
	s_waitcnt lgkmcnt(0)
	s_nop 0
	s_nop 1
	v_max_f32_dpp v55, v55, v55 row_bcast:15 row_mask:0xa bank_mask:0xf
	s_nop 0
	s_waitcnt lgkmcnt(0)
;     ...
;                 mx = fmaxf(wave_max(mx), 1e-30f); const float qs = 127.0f / mx;
; #pragma unroll
;                 for (int q = 0; q < 8; ++q) o4[64 * q] = pack_i8x4(v[q].x * qs, v[q].y * qs, v[q].z * qs, v[q].w * qs);
;                 if (lane == 0) ((float*)(ws + WS_ROWQ))[row] = mx * (1.0f / 127.0f); }
	s_nop 1
	v_max_f32_dpp v55, v55, v55 row_bcast:31 row_mask:0xc bank_mask:0xf
	s_nop 0
	v_readlane_b32 s98, v55, 63
	s_nop 1
	v_mov_b32_e32 v55, s98
	v_max_f32_e32 v55, s5, v55
	v_div_scale_f32 v88, s[2:3], v55, v55, s6
	v_rcp_f32_e32 v89, v88
	v_div_scale_f32 v90, vcc, s6, v55, s6
	v_fma_f32 v91, -v88, v89, 1.0
	v_fmac_f32_e32 v89, v91, v89
	v_mul_f32_e32 v91, v90, v89
	v_fma_f32 v92, -v88, v91, v90
	v_fmac_f32_e32 v91, v92, v89
	v_fma_f32 v88, -v88, v91, v90
	v_div_fmas_f32 v88, v88, v89, v91
	v_div_fixup_f32 v88, v88, v55, s6
	v_mul_f32_e32 v73, v73, v88
	v_mul_f32_e32 v72, v72, v88
	v_mul_f32_e32 v74, v74, v88
	v_mul_f32_e32 v75, v75, v88
	v_rndne_f32_e32 v73, v73
	v_rndne_f32_e32 v72, v72
	v_cvt_i32_f32_e32 v73, v73
	v_rndne_f32_e32 v74, v74
	v_rndne_f32_e32 v75, v75
	v_cvt_i32_f32_e32 v72, v72
	v_cvt_i32_f32_sdwa v74, v74 dst_sel:WORD_1 dst_unused:UNUSED_PAD src0_sel:DWORD
	v_cvt_i32_f32_e32 v75, v75
	v_lshlrev_b32_e32 v73, 8, v73
	v_and_b32_e32 v73, 0xff00, v73
	v_and_b32_e32 v74, 0xff0000, v74
	v_perm_b32 v72, v75, v72, s7
	v_or3_b32 v72, v72, v73, v74
	v_mul_f32_e32 v57, v57, v88
	global_store_dword v[42:43], v72, off offset:-1024
	v_mul_f32_e32 v56, v56, v88
	v_mul_f32_e32 v72, v76, v88
	v_mul_f32_e32 v73, v77, v88
	v_rndne_f32_e32 v57, v57
	v_rndne_f32_e32 v56, v56
	v_cvt_i32_f32_e32 v57, v57
	v_rndne_f32_e32 v72, v72
	v_rndne_f32_e32 v73, v73
	v_cvt_i32_f32_e32 v56, v56
	v_cvt_i32_f32_sdwa v72, v72 dst_sel:WORD_1 dst_unused:UNUSED_PAD src0_sel:DWORD
	v_cvt_i32_f32_e32 v73, v73
	v_lshlrev_b32_e32 v57, 8, v57
	v_and_b32_e32 v57, 0xff00, v57
	v_and_b32_e32 v72, 0xff0000, v72
	v_perm_b32 v56, v73, v56, s7
	v_or3_b32 v56, v56, v57, v72
	v_mul_f32_e32 v57, v59, v88
	global_store_dword v[42:43], v56, off offset:-768
	v_mul_f32_e32 v56, v58, v88
	v_mul_f32_e32 v58, v78, v88
	v_mul_f32_e32 v59, v79, v88
	v_rndne_f32_e32 v57, v57
	v_rndne_f32_e32 v56, v56
	v_cvt_i32_f32_e32 v57, v57
	v_rndne_f32_e32 v58, v58
	v_rndne_f32_e32 v59, v59
	v_cvt_i32_f32_e32 v56, v56
	v_cvt_i32_f32_sdwa v58, v58 dst_sel:WORD_1 dst_unused:UNUSED_PAD src0_sel:DWORD
	v_cvt_i32_f32_e32 v59, v59
	v_lshlrev_b32_e32 v57, 8, v57
	v_and_b32_e32 v57, 0xff00, v57
	v_and_b32_e32 v58, 0xff0000, v58
	v_perm_b32 v56, v59, v56, s7
	v_or3_b32 v56, v56, v57, v58
	v_mul_f32_e32 v57, v61, v88
	global_store_dword v[42:43], v56, off offset:-512
	v_mul_f32_e32 v56, v60, v88
	v_mul_f32_e32 v58, v80, v88
	v_mul_f32_e32 v59, v81, v88
	v_rndne_f32_e32 v57, v57
	v_rndne_f32_e32 v56, v56
	v_cvt_i32_f32_e32 v57, v57
	v_rndne_f32_e32 v58, v58
	v_rndne_f32_e32 v59, v59
	v_cvt_i32_f32_e32 v56, v56
	v_cvt_i32_f32_sdwa v58, v58 dst_sel:WORD_1 dst_unused:UNUSED_PAD src0_sel:DWORD
	v_cvt_i32_f32_e32 v59, v59
	v_lshlrev_b32_e32 v57, 8, v57
	v_and_b32_e32 v57, 0xff00, v57
	v_and_b32_e32 v58, 0xff0000, v58
	v_perm_b32 v56, v59, v56, s7
	v_or3_b32 v56, v56, v57, v58
	v_mul_f32_e32 v57, v63, v88
	global_store_dword v[42:43], v56, off offset:-256
	v_mul_f32_e32 v56, v62, v88
	v_mul_f32_e32 v58, v82, v88
	v_mul_f32_e32 v59, v83, v88
	v_rndne_f32_e32 v57, v57
	v_rndne_f32_e32 v56, v56
	v_cvt_i32_f32_e32 v57, v57
	v_rndne_f32_e32 v58, v58
	v_rndne_f32_e32 v59, v59
	v_cvt_i32_f32_e32 v56, v56
	v_cvt_i32_f32_sdwa v58, v58 dst_sel:WORD_1 dst_unused:UNUSED_PAD src0_sel:DWORD
	v_cvt_i32_f32_e32 v59, v59
	v_lshlrev_b32_e32 v57, 8, v57
	v_and_b32_e32 v57, 0xff00, v57
	v_and_b32_e32 v58, 0xff0000, v58
	v_perm_b32 v56, v59, v56, s7
	v_or3_b32 v56, v56, v57, v58
	v_mul_f32_e32 v57, v65, v88
	global_store_dword v[42:43], v56, off
	v_mul_f32_e32 v56, v64, v88
	v_mul_f32_e32 v58, v84, v88
	v_mul_f32_e32 v59, v85, v88
	v_rndne_f32_e32 v57, v57
	v_rndne_f32_e32 v56, v56
	v_cvt_i32_f32_e32 v57, v57
	v_rndne_f32_e32 v58, v58
	v_rndne_f32_e32 v59, v59
	v_cvt_i32_f32_e32 v56, v56
	v_cvt_i32_f32_sdwa v58, v58 dst_sel:WORD_1 dst_unused:UNUSED_PAD src0_sel:DWORD
	v_cvt_i32_f32_e32 v59, v59
	v_lshlrev_b32_e32 v57, 8, v57
	v_and_b32_e32 v57, 0xff00, v57
	v_and_b32_e32 v58, 0xff0000, v58
	v_perm_b32 v56, v59, v56, s7
	v_or3_b32 v56, v56, v57, v58
	v_mul_f32_e32 v57, v67, v88
	global_store_dword v[42:43], v56, off offset:256
	v_mul_f32_e32 v56, v66, v88
	v_mul_f32_e32 v58, v86, v88
	v_mul_f32_e32 v59, v87, v88
	v_rndne_f32_e32 v57, v57
	v_rndne_f32_e32 v56, v56
	v_cvt_i32_f32_e32 v57, v57
	v_rndne_f32_e32 v58, v58
	v_rndne_f32_e32 v59, v59
	v_cvt_i32_f32_e32 v56, v56
	v_cvt_i32_f32_sdwa v58, v58 dst_sel:WORD_1 dst_unused:UNUSED_PAD src0_sel:DWORD
	v_cvt_i32_f32_e32 v59, v59
	v_lshlrev_b32_e32 v57, 8, v57
	v_and_b32_e32 v57, 0xff00, v57
	v_and_b32_e32 v58, 0xff0000, v58
	v_perm_b32 v56, v59, v56, s7
	v_or3_b32 v56, v56, v57, v58
	v_mul_f32_e32 v57, v69, v88
	global_store_dword v[42:43], v56, off offset:512
	v_mul_f32_e32 v56, v68, v88
	v_mul_f32_e32 v58, v70, v88
	v_mul_f32_e32 v59, v71, v88
	v_rndne_f32_e32 v57, v57
	v_rndne_f32_e32 v56, v56
	v_cvt_i32_f32_e32 v57, v57
	v_rndne_f32_e32 v58, v58
	v_rndne_f32_e32 v59, v59
	v_cvt_i32_f32_e32 v56, v56
	v_cvt_i32_f32_sdwa v58, v58 dst_sel:WORD_1 dst_unused:UNUSED_PAD src0_sel:DWORD
	v_cvt_i32_f32_e32 v59, v59
	v_lshlrev_b32_e32 v57, 8, v57
	v_and_b32_e32 v57, 0xff00, v57
	v_and_b32_e32 v58, 0xff0000, v58
	v_perm_b32 v56, v59, v56, s7
	v_or3_b32 v56, v56, v57, v58
	global_store_dword v[42:43], v56, off offset:768
	s_and_saveexec_b64 s[2:3], s[0:1]
	s_cbranch_execz .LBB0_769
	v_mul_f32_e32 v55, 0x3c010204, v55
	global_store_dword v[46:47], v55, off
	s_branch .LBB0_769

; template <bool SB> __device__ __forceinline__ void load_row(const void* xin, size_t row, int lane, f32x4 (&v)[8]) {
;     if (SB) { typedef _Float16 h16x4_t __attribute__((ext_vector_type(4))); const h16x4_t* xr = (const h16x4_t*)((const bf16*)xin + row * DM) + lane;
; #pragma unroll
;         for (int q = 0; q < 8; ++q) { const h16x4_t w = xr[64 * q]; v[q] = (f32x4){(float)w[0], (float)w[1], (float)w[2], (float)w[3]}; } }
;     ...
;             f32x4 v[8]; float ss = 0.f; load_row<SB>(xin, (size_t)row, lane, v);
; #pragma unroll
;             for (int q = 0; q < 8; ++q) ss += (v[q].x * v[q].x + v[q].y * v[q].y) + (v[q].z * v[q].z + v[q].w * v[q].w);
;             const float rstd = 1.0f / sqrtf(wave_sum(ss) * (1.0f / DM) + NORM_EPS);
.LBB0_1124:
	global_load_dwordx2 v[56:57], v[38:39], off offset:-3584
	global_load_dwordx2 v[58:59], v[38:39], off offset:-3072
	global_load_dwordx2 v[60:61], v[38:39], off offset:-2560
	global_load_dwordx2 v[62:63], v[38:39], off offset:-2048
	global_load_dwordx2 v[64:65], v[38:39], off offset:-1536
	global_load_dwordx2 v[66:67], v[38:39], off offset:-1024
	global_load_dwordx2 v[68:69], v[38:39], off offset:-512
	global_load_dwordx2 v[70:71], v[38:39], off
	s_waitcnt vmcnt(7)
	v_cvt_f32_f16_sdwa v73, v56 dst_sel:DWORD dst_unused:UNUSED_PAD src0_sel:WORD_1
	v_cvt_f32_f16_sdwa v75, v57 dst_sel:DWORD dst_unused:UNUSED_PAD src0_sel:WORD_1
	v_cvt_f32_f16_e32 v74, v57
	s_waitcnt vmcnt(6)
	v_cvt_f32_f16_sdwa v57, v58 dst_sel:DWORD dst_unused:UNUSED_PAD src0_sel:WORD_1
	v_cvt_f32_f16_sdwa v77, v59 dst_sel:DWORD dst_unused:UNUSED_PAD src0_sel:WORD_1
	v_cvt_f32_f16_e32 v72, v56
	v_cvt_f32_f16_e32 v56, v58
	v_cvt_f32_f16_e32 v76, v59
	s_waitcnt vmcnt(5)
	v_cvt_f32_f16_sdwa v59, v60 dst_sel:DWORD dst_unused:UNUSED_PAD src0_sel:WORD_1
	v_cvt_f32_f16_sdwa v79, v61 dst_sel:DWORD dst_unused:UNUSED_PAD src0_sel:WORD_1
	v_cvt_f32_f16_e32 v58, v60
	v_cvt_f32_f16_e32 v78, v61
	s_waitcnt vmcnt(4)
	v_cvt_f32_f16_sdwa v61, v62 dst_sel:DWORD dst_unused:UNUSED_PAD src0_sel:WORD_1
	v_cvt_f32_f16_sdwa v81, v63 dst_sel:DWORD dst_unused:UNUSED_PAD src0_sel:WORD_1
	v_cvt_f32_f16_e32 v60, v62
	v_cvt_f32_f16_e32 v80, v63
	s_waitcnt vmcnt(3)
	v_cvt_f32_f16_sdwa v63, v64 dst_sel:DWORD dst_unused:UNUSED_PAD src0_sel:WORD_1
	v_cvt_f32_f16_e32 v62, v64
	v_cvt_f32_f16_sdwa v83, v65 dst_sel:DWORD dst_unused:UNUSED_PAD src0_sel:WORD_1
	v_cvt_f32_f16_e32 v82, v65
	v_mov_b32_e32 v90, v73
	v_mov_b32_e32 v91, v57
	v_mov_b32_e32 v94, v75
	v_mov_b32_e32 v95, v77
	s_waitcnt vmcnt(2)
	v_cvt_f32_f16_sdwa v65, v66 dst_sel:DWORD dst_unused:UNUSED_PAD src0_sel:WORD_1
	v_cvt_f32_f16_e32 v64, v66
	v_cvt_f32_f16_sdwa v85, v67 dst_sel:DWORD dst_unused:UNUSED_PAD src0_sel:WORD_1
	v_cvt_f32_f16_e32 v84, v67
	s_waitcnt vmcnt(1)
	v_cvt_f32_f16_sdwa v67, v68 dst_sel:DWORD dst_unused:UNUSED_PAD src0_sel:WORD_1
	v_cvt_f32_f16_e32 v66, v68
	v_cvt_f32_f16_sdwa v87, v69 dst_sel:DWORD dst_unused:UNUSED_PAD src0_sel:WORD_1
	v_cvt_f32_f16_e32 v86, v69
	s_waitcnt vmcnt(0)
	v_cvt_f32_f16_sdwa v69, v70 dst_sel:DWORD dst_unused:UNUSED_PAD src0_sel:WORD_1
	v_cvt_f32_f16_e32 v68, v70
	v_cvt_f32_f16_sdwa v89, v71 dst_sel:DWORD dst_unused:UNUSED_PAD src0_sel:WORD_1
	v_cvt_f32_f16_e32 v88, v71
	v_mov_b32_e32 v70, v72
	v_mov_b32_e32 v71, v56
	v_mov_b32_e32 v92, v74
	v_mov_b32_e32 v93, v76
	v_mov_b32_e32 v98, v59
	v_mov_b32_e32 v99, v79
	v_pk_mul_f32 v[90:91], v[90:91], v[90:91]
	v_pk_mul_f32 v[94:95], v[94:95], v[94:95]
	v_mov_b32_e32 v96, v58
	v_mov_b32_e32 v97, v78
	v_pk_mul_f32 v[98:99], v[98:99], v[98:99]
	v_pk_fma_f32 v[70:71], v[70:71], v[70:71], v[90:91]
	v_pk_fma_f32 v[90:91], v[92:93], v[92:93], v[94:95]
	v_mul_f32_e32 v100, v61, v61
	v_mul_f32_e32 v102, v81, v81
	v_pk_fma_f32 v[92:93], v[96:97], v[96:97], v[98:99]
	v_pk_add_f32 v[70:71], v[70:71], v[90:91]
	v_pk_mul_f32 v[104:105], v[62:63], v[62:63]
	v_pk_mul_f32 v[106:107], v[82:83], v[82:83]
	v_pk_fma_f32 v[100:101], v[60:61], v[60:61], v[100:101] op_sel_hi:[1,1,0]
	v_pk_fma_f32 v[102:103], v[80:81], v[80:81], v[102:103] op_sel_hi:[1,1,0]
	v_pk_add_f32 v[90:91], v[92:93], v[92:93] op_sel:[0,1] op_sel_hi:[1,0]
	v_pk_add_f32 v[70:71], v[70:71], v[70:71] op_sel:[0,1] op_sel_hi:[1,0]
	v_mov_b32_e32 v110, v65
	v_mov_b32_e32 v111, v85
	v_mov_b32_e32 v101, v106
	v_mov_b32_e32 v103, v107
	v_mov_b32_e32 v91, v105
	v_mov_b32_e32 v71, v104
	v_mov_b32_e32 v108, v64
	v_mov_b32_e32 v109, v84
	v_pk_mul_f32 v[110:111], v[110:111], v[110:111]
	v_pk_add_f32 v[92:93], v[100:101], v[102:103]
	v_pk_add_f32 v[70:71], v[70:71], v[90:91]
	v_mul_f32_e32 v112, v67, v67
	v_mul_f32_e32 v114, v87, v87
	v_pk_fma_f32 v[94:95], v[108:109], v[108:109], v[110:111]
	v_pk_add_f32 v[70:71], v[70:71], v[92:93]
	v_pk_mul_f32 v[116:117], v[68:69], v[68:69]
	v_pk_mul_f32 v[118:119], v[88:89], v[88:89]
	v_pk_fma_f32 v[112:113], v[66:67], v[66:67], v[112:113] op_sel_hi:[1,1,0]
	v_pk_fma_f32 v[114:115], v[86:87], v[86:87], v[114:115] op_sel_hi:[1,1,0]
	v_pk_add_f32 v[94:95], v[94:95], v[94:95] op_sel:[0,1] op_sel_hi:[1,0]
	v_pk_add_f32 v[70:71], v[70:71], v[70:71] op_sel:[0,1] op_sel_hi:[1,0]
	v_mov_b32_e32 v113, v118
	v_mov_b32_e32 v115, v119
	v_mov_b32_e32 v95, v117
	v_mov_b32_e32 v71, v116
	v_pk_add_f32 v[96:97], v[112:113], v[114:115]
	v_pk_add_f32 v[70:71], v[70:71], v[94:95]
	s_nop 0
	v_pk_add_f32 v[70:71], v[70:71], v[96:97]
	s_nop 0
	v_add_f32_e32 v55, v70, v71
	s_nop 0
	s_waitcnt lgkmcnt(0)
	s_nop 1
	v_add_f32_dpp v55, v55, v55 quad_perm:[1,0,3,2] row_mask:0xf bank_mask:0xf bound_ctrl:1
	s_nop 0
	s_waitcnt lgkmcnt(0)
	s_nop 1
	v_add_f32_dpp v55, v55, v55 quad_perm:[2,3,0,1] row_mask:0xf bank_mask:0xf bound_ctrl:1
	s_nop 0
	s_waitcnt lgkmcnt(0)
	s_nop 1
	v_add_f32_dpp v55, v55, v55 row_half_mirror row_mask:0xf bank_mask:0xf bound_ctrl:1
	s_nop 0
	s_waitcnt lgkmcnt(0)
	s_nop 1
	v_add_f32_dpp v55, v55, v55 row_mirror row_mask:0xf bank_mask:0xf bound_ctrl:1
	s_nop 0
	s_waitcnt lgkmcnt(0)
	s_nop 1
	v_add_f32_dpp v55, v55, v55 row_bcast:15 row_mask:0xa bank_mask:0xf
	s_nop 0
	s_waitcnt lgkmcnt(0)
; __device__ __forceinline__ float wave_max(float v) {
; #pragma unroll
;     for (int o = 1; o < 64; o <<= 1) v = fmaxf(v, __shfl_xor(v, o));
;     return v;
; }
;     ...
;             const float rstd = 1.0f / sqrtf(wave_sum(ss) * (1.0f / DM) + NORM_EPS);
;             if (F8 == 2) { unsigned* o4 = (unsigned*)((unsigned char*)xn + (size_t)row * DM) + lane; float mx = 0.f;
; #pragma unroll
;                 for (int q = 0; q < 8; ++q) { v[q] = v[q] * rstd * gn[q]; mx = fmaxf(fmaxf(mx, fmaxf(fabsf(v[q].x), fabsf(v[q].y))), fmaxf(fabsf(v[q].z), fabsf(v[q].w))); }
;                 mx = fmaxf(wave_max(mx), 1e-30f); const float qs = 127.0f / mx;
	s_nop 1
	v_add_f32_dpp v55, v55, v55 row_bcast:31 row_mask:0xc bank_mask:0xf
	s_nop 0
	v_readlane_b32 s98, v55, 63
	s_nop 1
	v_mov_b32_e32 v55, s98
	v_fmamk_f32 v55, v55, 0x3a000000, v53
	v_mul_f32_e32 v70, 0x4f800000, v55
	v_cmp_gt_f32_e32 vcc, s4, v55
	s_nop 1
	v_cndmask_b32_e32 v55, v55, v70, vcc
	v_sqrt_f32_e32 v70, v55
	s_nop 0
	v_add_u32_e32 v71, -1, v70
	v_add_u32_e32 v90, 1, v70
	v_fma_f32 v91, -v71, v70, v55
	v_fma_f32 v92, -v90, v70, v55
	v_cmp_ge_f32_e64 s[2:3], 0, v91
	s_nop 1
	v_cndmask_b32_e64 v70, v70, v71, s[2:3]
	v_cmp_lt_f32_e64 s[2:3], 0, v92
	s_nop 1
	v_cndmask_b32_e64 v70, v70, v90, s[2:3]
	v_mul_f32_e32 v71, 0x37800000, v70
	v_cndmask_b32_e32 v70, v70, v71, vcc
	v_cmp_class_f32_e32 vcc, v55, v54
	s_nop 1
	v_cndmask_b32_e32 v55, v70, v55, vcc
	v_div_scale_f32 v70, s[2:3], v55, v55, 1.0
	v_rcp_f32_e32 v71, v70
	v_div_scale_f32 v90, vcc, 1.0, v55, 1.0
	v_fma_f32 v91, -v70, v71, 1.0
	v_fmac_f32_e32 v71, v91, v71
	v_mul_f32_e32 v91, v90, v71
	v_fma_f32 v92, -v70, v91, v90
	v_fmac_f32_e32 v91, v92, v71
	v_fma_f32 v70, -v70, v91, v90
	v_div_fmas_f32 v70, v70, v71, v91
	v_div_fixup_f32 v70, v70, v55, 1.0
	v_pk_mul_f32 v[74:75], v[74:75], v[70:71] op_sel_hi:[1,0]
	v_pk_mul_f32 v[72:73], v[72:73], v[70:71] op_sel_hi:[1,0]
	v_pk_mul_f32 v[74:75], v[12:13], v[74:75]
	v_pk_mul_f32 v[56:57], v[56:57], v[70:71] op_sel_hi:[1,0]
	v_pk_mul_f32 v[76:77], v[76:77], v[70:71] op_sel_hi:[1,0]
	v_pk_mul_f32 v[58:59], v[58:59], v[70:71] op_sel_hi:[1,0]
	v_pk_mul_f32 v[78:79], v[78:79], v[70:71] op_sel_hi:[1,0]
	v_pk_mul_f32 v[60:61], v[60:61], v[70:71] op_sel_hi:[1,0]
	v_pk_mul_f32 v[80:81], v[80:81], v[70:71] op_sel_hi:[1,0]
	v_pk_mul_f32 v[72:73], v[10:11], v[72:73]
	v_max_f32_e64 v71, |v74|, |v75|
	v_pk_mul_f32 v[76:77], v[4:5], v[76:77]
	v_pk_mul_f32 v[56:57], v[2:3], v[56:57]
	v_max_f32_e64 v55, |v72|, |v73|
	v_pk_mul_f32 v[62:63], v[62:63], v[70:71] op_sel_hi:[1,0]
	v_pk_mul_f32 v[78:79], v[8:9], v[78:79]
	v_pk_mul_f32 v[58:59], v[6:7], v[58:59]
	v_max_f32_e64 v90, |v56|, |v57|
	v_max_f32_e64 v91, |v76|, |v77|
	v_max3_f32 v55, v55, 0, v71
	v_pk_mul_f32 v[62:63], v[18:19], v[62:63]
	v_pk_mul_f32 v[80:81], v[16:17], v[80:81]
	v_pk_mul_f32 v[60:61], v[14:15], v[60:61]
	v_max_f32_e64 v92, |v58|, |v59|
	v_max_f32_e64 v93, |v78|, |v79|
	v_max3_f32 v55, v55, v90, v91
	v_pk_mul_f32 v[82:83], v[82:83], v[70:71] op_sel_hi:[1,0]
	v_max_f32_e64 v71, |v62|, |v63|
	v_max_f32_e64 v94, |v60|, |v61|
	v_max_f32_e64 v95, |v80|, |v81|
	v_max3_f32 v55, v55, v92, v93
	v_pk_mul_f32 v[82:83], v[20:21], v[82:83]
	v_pk_mul_f32 v[64:65], v[64:65], v[70:71] op_sel_hi:[1,0]
	v_max3_f32 v55, v55, v94, v95
	v_max_f32_e64 v90, |v82|, |v83|
	v_pk_mul_f32 v[64:65], v[22:23], v[64:65]
	v_max3_f32 v55, v55, v71, v90
	v_pk_mul_f32 v[84:85], v[84:85], v[70:71] op_sel_hi:[1,0]
	v_max_f32_e64 v71, |v64|, |v65|
	v_pk_mul_f32 v[84:85], v[24:25], v[84:85]
	v_pk_mul_f32 v[66:67], v[66:67], v[70:71] op_sel_hi:[1,0]
	v_pk_mul_f32 v[86:87], v[86:87], v[70:71] op_sel_hi:[1,0]
	v_max_f32_e64 v90, |v84|, |v85|
	v_pk_mul_f32 v[86:87], v[28:29], v[86:87]
	v_pk_mul_f32 v[66:67], v[26:27], v[66:67]
	v_max3_f32 v55, v55, v71, v90
	v_max_f32_e64 v71, |v66|, |v67|
	v_max_f32_e64 v90, |v86|, |v87|
	v_max3_f32 v55, v55, v71, v90
	v_pk_mul_f32 v[68:69], v[68:69], v[70:71] op_sel_hi:[1,0]
	v_pk_mul_f32 v[70:71], v[88:89], v[70:71] op_sel_hi:[1,0]
	v_pk_mul_f32 v[68:69], v[30:31], v[68:69]
	v_pk_mul_f32 v[70:71], v[32:33], v[70:71]
	v_max_f32_e64 v88, |v68|, |v69|
	v_max_f32_e64 v89, |v70|, |v71|
	v_max3_f32 v55, v55, v88, v89
	s_nop 0
	s_waitcnt lgkmcnt(0)
	s_nop 0
	s_nop 1
	v_max_f32_dpp v55, v55, v55 quad_perm:[1,0,3,2] row_mask:0xf bank_mask:0xf bound_ctrl:1
	s_nop 0
	s_waitcnt lgkmcnt(0)
	s_nop 0
	s_nop 1
	v_max_f32_dpp v55, v55, v55 quad_perm:[2,3,0,1] row_mask:0xf bank_mask:0xf bound_ctrl:1
	s_nop 0
	s_waitcnt lgkmcnt(0)
	s_nop 0
	s_nop 1
	v_max_f32_dpp v55, v55, v55 row_half_mirror row_mask:0xf bank_mask:0xf bound_ctrl:1
	s_nop 0
	s_waitcnt lgkmcnt(0)
	s_nop 0
	s_nop 1
	v_max_f32_dpp v55, v55, v55 row_mirror row_mask:0xf bank_mask:0xf bound_ctrl:1
	s_nop 0
	s_waitcnt lgkmcnt(0)
	s_nop 0
	s_nop 1
	v_max_f32_dpp v55, v55, v55 row_bcast:15 row_mask:0xa bank_mask:0xf
	s_nop 0
	s_waitcnt lgkmcnt(0)
;     ...
;                 mx = fmaxf(wave_max(mx), 1e-30f); const float qs = 127.0f / mx;
; #pragma unroll
;                 for (int q = 0; q < 8; ++q) o4[64 * q] = pack_i8x4(v[q].x * qs, v[q].y * qs, v[q].z * qs, v[q].w * qs);
;                 if (lane == 0) ((float*)(ws + WS_ROWQ))[row] = mx * (1.0f / 127.0f); }
	s_nop 1
	v_max_f32_dpp v55, v55, v55 row_bcast:31 row_mask:0xc bank_mask:0xf
	s_nop 0
	v_readlane_b32 s98, v55, 63
	s_nop 1
	v_mov_b32_e32 v55, s98
	v_max_f32_e32 v55, s5, v55
	v_div_scale_f32 v88, s[2:3], v55, v55, s6
	v_rcp_f32_e32 v89, v88
	v_div_scale_f32 v90, vcc, s6, v55, s6
	v_fma_f32 v91, -v88, v89, 1.0
	v_fmac_f32_e32 v89, v91, v89
	v_mul_f32_e32 v91, v90, v89
	v_fma_f32 v92, -v88, v91, v90
	v_fmac_f32_e32 v91, v92, v89
	v_fma_f32 v88, -v88, v91, v90
	v_div_fmas_f32 v88, v88, v89, v91
	v_div_fixup_f32 v88, v88, v55, s6
	v_mul_f32_e32 v73, v73, v88
	v_mul_f32_e32 v72, v72, v88
	v_mul_f32_e32 v74, v74, v88
	v_mul_f32_e32 v75, v75, v88
	v_rndne_f32_e32 v73, v73
	v_rndne_f32_e32 v72, v72
	v_cvt_i32_f32_e32 v73, v73
	v_rndne_f32_e32 v74, v74
	v_rndne_f32_e32 v75, v75
	v_cvt_i32_f32_e32 v72, v72
	v_cvt_i32_f32_sdwa v74, v74 dst_sel:WORD_1 dst_unused:UNUSED_PAD src0_sel:DWORD
	v_cvt_i32_f32_e32 v75, v75
	v_lshlrev_b32_e32 v73, 8, v73
	v_and_b32_e32 v73, 0xff00, v73
	v_and_b32_e32 v74, 0xff0000, v74
	v_perm_b32 v72, v75, v72, s7
	v_or3_b32 v72, v72, v73, v74
	v_mul_f32_e32 v57, v57, v88
	global_store_dword v[42:43], v72, off offset:-1024
	v_mul_f32_e32 v56, v56, v88
	v_mul_f32_e32 v72, v76, v88
	v_mul_f32_e32 v73, v77, v88
	v_rndne_f32_e32 v57, v57
	v_rndne_f32_e32 v56, v56
	v_cvt_i32_f32_e32 v57, v57
	v_rndne_f32_e32 v72, v72
	v_rndne_f32_e32 v73, v73
	v_cvt_i32_f32_e32 v56, v56
	v_cvt_i32_f32_sdwa v72, v72 dst_sel:WORD_1 dst_unused:UNUSED_PAD src0_sel:DWORD
	v_cvt_i32_f32_e32 v73, v73
	v_lshlrev_b32_e32 v57, 8, v57
	v_and_b32_e32 v57, 0xff00, v57
	v_and_b32_e32 v72, 0xff0000, v72
	v_perm_b32 v56, v73, v56, s7
	v_or3_b32 v56, v56, v57, v72
	v_mul_f32_e32 v57, v59, v88
	global_store_dword v[42:43], v56, off offset:-768
	v_mul_f32_e32 v56, v58, v88
	v_mul_f32_e32 v58, v78, v88
	v_mul_f32_e32 v59, v79, v88
	v_rndne_f32_e32 v57, v57
	v_rndne_f32_e32 v56, v56
	v_cvt_i32_f32_e32 v57, v57
	v_rndne_f32_e32 v58, v58
	v_rndne_f32_e32 v59, v59
	v_cvt_i32_f32_e32 v56, v56
	v_cvt_i32_f32_sdwa v58, v58 dst_sel:WORD_1 dst_unused:UNUSED_PAD src0_sel:DWORD
	v_cvt_i32_f32_e32 v59, v59
	v_lshlrev_b32_e32 v57, 8, v57
	v_and_b32_e32 v57, 0xff00, v57
	v_and_b32_e32 v58, 0xff0000, v58
	v_perm_b32 v56, v59, v56, s7
	v_or3_b32 v56, v56, v57, v58
	v_mul_f32_e32 v57, v61, v88
	global_store_dword v[42:43], v56, off offset:-512
	v_mul_f32_e32 v56, v60, v88
	v_mul_f32_e32 v58, v80, v88
	v_mul_f32_e32 v59, v81, v88
	v_rndne_f32_e32 v57, v57
	v_rndne_f32_e32 v56, v56
	v_cvt_i32_f32_e32 v57, v57
	v_rndne_f32_e32 v58, v58
	v_rndne_f32_e32 v59, v59
	v_cvt_i32_f32_e32 v56, v56
	v_cvt_i32_f32_sdwa v58, v58 dst_sel:WORD_1 dst_unused:UNUSED_PAD src0_sel:DWORD
	v_cvt_i32_f32_e32 v59, v59
	v_lshlrev_b32_e32 v57, 8, v57
	v_and_b32_e32 v57, 0xff00, v57
	v_and_b32_e32 v58, 0xff0000, v58
	v_perm_b32 v56, v59, v56, s7
	v_or3_b32 v56, v56, v57, v58
	v_mul_f32_e32 v57, v63, v88
	global_store_dword v[42:43], v56, off offset:-256
	v_mul_f32_e32 v56, v62, v88
	v_mul_f32_e32 v58, v82, v88
	v_mul_f32_e32 v59, v83, v88
	v_rndne_f32_e32 v57, v57
	v_rndne_f32_e32 v56, v56
	v_cvt_i32_f32_e32 v57, v57
	v_rndne_f32_e32 v58, v58
	v_rndne_f32_e32 v59, v59
	v_cvt_i32_f32_e32 v56, v56
	v_cvt_i32_f32_sdwa v58, v58 dst_sel:WORD_1 dst_unused:UNUSED_PAD src0_sel:DWORD
	v_cvt_i32_f32_e32 v59, v59
	v_lshlrev_b32_e32 v57, 8, v57
	v_and_b32_e32 v57, 0xff00, v57
	v_and_b32_e32 v58, 0xff0000, v58
	v_perm_b32 v56, v59, v56, s7
	v_or3_b32 v56, v56, v57, v58
	v_mul_f32_e32 v57, v65, v88
	global_store_dword v[42:43], v56, off
	v_mul_f32_e32 v56, v64, v88
	v_mul_f32_e32 v58, v84, v88
	v_mul_f32_e32 v59, v85, v88
	v_rndne_f32_e32 v57, v57
	v_rndne_f32_e32 v56, v56
	v_cvt_i32_f32_e32 v57, v57
	v_rndne_f32_e32 v58, v58
	v_rndne_f32_e32 v59, v59
	v_cvt_i32_f32_e32 v56, v56
	v_cvt_i32_f32_sdwa v58, v58 dst_sel:WORD_1 dst_unused:UNUSED_PAD src0_sel:DWORD
	v_cvt_i32_f32_e32 v59, v59
	v_lshlrev_b32_e32 v57, 8, v57
	v_and_b32_e32 v57, 0xff00, v57
	v_and_b32_e32 v58, 0xff0000, v58
	v_perm_b32 v56, v59, v56, s7
	v_or3_b32 v56, v56, v57, v58
	v_mul_f32_e32 v57, v67, v88
	global_store_dword v[42:43], v56, off offset:256
	v_mul_f32_e32 v56, v66, v88
	v_mul_f32_e32 v58, v86, v88
	v_mul_f32_e32 v59, v87, v88
	v_rndne_f32_e32 v57, v57
	v_rndne_f32_e32 v56, v56
	v_cvt_i32_f32_e32 v57, v57
	v_rndne_f32_e32 v58, v58
	v_rndne_f32_e32 v59, v59
	v_cvt_i32_f32_e32 v56, v56
	v_cvt_i32_f32_sdwa v58, v58 dst_sel:WORD_1 dst_unused:UNUSED_PAD src0_sel:DWORD
	v_cvt_i32_f32_e32 v59, v59
	v_lshlrev_b32_e32 v57, 8, v57
	v_and_b32_e32 v57, 0xff00, v57
	v_and_b32_e32 v58, 0xff0000, v58
	v_perm_b32 v56, v59, v56, s7
	v_or3_b32 v56, v56, v57, v58
	v_mul_f32_e32 v57, v69, v88
	global_store_dword v[42:43], v56, off offset:512
	v_mul_f32_e32 v56, v68, v88
	v_mul_f32_e32 v58, v70, v88
	v_mul_f32_e32 v59, v71, v88
	v_rndne_f32_e32 v57, v57
	v_rndne_f32_e32 v56, v56
	v_cvt_i32_f32_e32 v57, v57
	v_rndne_f32_e32 v58, v58
	v_rndne_f32_e32 v59, v59
	v_cvt_i32_f32_e32 v56, v56
	v_cvt_i32_f32_sdwa v58, v58 dst_sel:WORD_1 dst_unused:UNUSED_PAD src0_sel:DWORD
	v_cvt_i32_f32_e32 v59, v59
	v_lshlrev_b32_e32 v57, 8, v57
	v_and_b32_e32 v57, 0xff00, v57
	v_and_b32_e32 v58, 0xff0000, v58
	v_perm_b32 v56, v59, v56, s7
	v_or3_b32 v56, v56, v57, v58
	global_store_dword v[42:43], v56, off offset:768
	s_and_saveexec_b64 s[2:3], s[0:1]
	s_cbranch_execz .LBB0_1123
	v_mul_f32_e32 v55, 0x3c010204, v55
	global_store_dword v[46:47], v55, off
	s_branch .LBB0_1123

; template <bool SB> __device__ __forceinline__ void load_row(const void* xin, size_t row, int lane, f32x4 (&v)[8]) {
;     if (SB) { typedef _Float16 h16x4_t __attribute__((ext_vector_type(4))); const h16x4_t* xr = (const h16x4_t*)((const bf16*)xin + row * DM) + lane;
; #pragma unroll
;         for (int q = 0; q < 8; ++q) { const h16x4_t w = xr[64 * q]; v[q] = (f32x4){(float)w[0], (float)w[1], (float)w[2], (float)w[3]}; } }
;     ...
;             f32x4 v[8]; float ss = 0.f; load_row<SB>(xin, (size_t)row, lane, v);
; #pragma unroll
;             for (int q = 0; q < 8; ++q) ss += (v[q].x * v[q].x + v[q].y * v[q].y) + (v[q].z * v[q].z + v[q].w * v[q].w);
;             const float rstd = 1.0f / sqrtf(wave_sum(ss) * (1.0f / DM) + NORM_EPS);
.LBB0_1334:
	global_load_dwordx2 v[62:63], v[46:47], off offset:-2048
	global_load_dwordx2 v[64:65], v[46:47], off offset:-1536
	global_load_dwordx2 v[66:67], v[46:47], off offset:-1024
	global_load_dwordx2 v[68:69], v[46:47], off offset:-512
	global_load_dwordx2 v[70:71], v[46:47], off
	global_load_dwordx2 v[72:73], v[46:47], off offset:512
	global_load_dwordx2 v[74:75], v[46:47], off offset:1024
	global_load_dwordx2 v[76:77], v[46:47], off offset:1536
	s_waitcnt vmcnt(7)
	v_cvt_f32_f16_sdwa v79, v62 dst_sel:DWORD dst_unused:UNUSED_PAD src0_sel:WORD_1
	v_cvt_f32_f16_sdwa v81, v63 dst_sel:DWORD dst_unused:UNUSED_PAD src0_sel:WORD_1
	v_cvt_f32_f16_e32 v80, v63
	s_waitcnt vmcnt(6)
	v_cvt_f32_f16_sdwa v63, v64 dst_sel:DWORD dst_unused:UNUSED_PAD src0_sel:WORD_1
	v_cvt_f32_f16_sdwa v83, v65 dst_sel:DWORD dst_unused:UNUSED_PAD src0_sel:WORD_1
	v_cvt_f32_f16_e32 v78, v62
	v_cvt_f32_f16_e32 v62, v64
	v_cvt_f32_f16_e32 v82, v65
	s_waitcnt vmcnt(5)
	v_cvt_f32_f16_sdwa v65, v66 dst_sel:DWORD dst_unused:UNUSED_PAD src0_sel:WORD_1
	v_cvt_f32_f16_sdwa v85, v67 dst_sel:DWORD dst_unused:UNUSED_PAD src0_sel:WORD_1
	v_cvt_f32_f16_e32 v64, v66
	v_cvt_f32_f16_e32 v84, v67
	s_waitcnt vmcnt(4)
	v_cvt_f32_f16_sdwa v67, v68 dst_sel:DWORD dst_unused:UNUSED_PAD src0_sel:WORD_1
	v_cvt_f32_f16_sdwa v87, v69 dst_sel:DWORD dst_unused:UNUSED_PAD src0_sel:WORD_1
	v_cvt_f32_f16_e32 v66, v68
	v_cvt_f32_f16_e32 v86, v69
	s_waitcnt vmcnt(3)
	v_cvt_f32_f16_sdwa v69, v70 dst_sel:DWORD dst_unused:UNUSED_PAD src0_sel:WORD_1
	v_cvt_f32_f16_e32 v68, v70
	v_cvt_f32_f16_sdwa v89, v71 dst_sel:DWORD dst_unused:UNUSED_PAD src0_sel:WORD_1
	v_cvt_f32_f16_e32 v88, v71
	v_mov_b32_e32 v96, v79
	v_mov_b32_e32 v97, v63
	v_mov_b32_e32 v100, v81
	v_mov_b32_e32 v101, v83
	s_waitcnt vmcnt(2)
	v_cvt_f32_f16_sdwa v71, v72 dst_sel:DWORD dst_unused:UNUSED_PAD src0_sel:WORD_1
	v_cvt_f32_f16_e32 v70, v72
	v_cvt_f32_f16_sdwa v91, v73 dst_sel:DWORD dst_unused:UNUSED_PAD src0_sel:WORD_1
	v_cvt_f32_f16_e32 v90, v73
	s_waitcnt vmcnt(1)
	v_cvt_f32_f16_sdwa v73, v74 dst_sel:DWORD dst_unused:UNUSED_PAD src0_sel:WORD_1
	v_cvt_f32_f16_e32 v72, v74
	v_cvt_f32_f16_sdwa v93, v75 dst_sel:DWORD dst_unused:UNUSED_PAD src0_sel:WORD_1
	v_cvt_f32_f16_e32 v92, v75
	s_waitcnt vmcnt(0)
	v_cvt_f32_f16_sdwa v75, v76 dst_sel:DWORD dst_unused:UNUSED_PAD src0_sel:WORD_1
	v_cvt_f32_f16_e32 v74, v76
	v_cvt_f32_f16_sdwa v95, v77 dst_sel:DWORD dst_unused:UNUSED_PAD src0_sel:WORD_1
	v_cvt_f32_f16_e32 v94, v77
	v_mov_b32_e32 v76, v78
	v_mov_b32_e32 v77, v62
	v_mov_b32_e32 v98, v80
	v_mov_b32_e32 v99, v82
	v_mov_b32_e32 v104, v65
	v_mov_b32_e32 v105, v85
	v_pk_mul_f32 v[96:97], v[96:97], v[96:97]
	v_pk_mul_f32 v[100:101], v[100:101], v[100:101]
	v_mov_b32_e32 v102, v64
	v_mov_b32_e32 v103, v84
	v_pk_mul_f32 v[104:105], v[104:105], v[104:105]
	v_pk_fma_f32 v[76:77], v[76:77], v[76:77], v[96:97]
	v_pk_fma_f32 v[96:97], v[98:99], v[98:99], v[100:101]
	v_mul_f32_e32 v106, v67, v67
	v_mul_f32_e32 v108, v87, v87
	v_pk_fma_f32 v[98:99], v[102:103], v[102:103], v[104:105]
	v_pk_add_f32 v[76:77], v[76:77], v[96:97]
	v_pk_mul_f32 v[110:111], v[68:69], v[68:69]
	v_pk_mul_f32 v[112:113], v[88:89], v[88:89]
	v_pk_fma_f32 v[106:107], v[66:67], v[66:67], v[106:107] op_sel_hi:[1,1,0]
	v_pk_fma_f32 v[108:109], v[86:87], v[86:87], v[108:109] op_sel_hi:[1,1,0]
	v_pk_add_f32 v[96:97], v[98:99], v[98:99] op_sel:[0,1] op_sel_hi:[1,0]
	v_pk_add_f32 v[76:77], v[76:77], v[76:77] op_sel:[0,1] op_sel_hi:[1,0]
	v_mov_b32_e32 v116, v71
	v_mov_b32_e32 v117, v91
	v_mov_b32_e32 v107, v112
	v_mov_b32_e32 v109, v113
	v_mov_b32_e32 v97, v111
	v_mov_b32_e32 v77, v110
	v_mov_b32_e32 v114, v70
	v_mov_b32_e32 v115, v90
	v_pk_mul_f32 v[116:117], v[116:117], v[116:117]
	v_pk_add_f32 v[98:99], v[106:107], v[108:109]
	v_pk_add_f32 v[76:77], v[76:77], v[96:97]
	v_mul_f32_e32 v118, v73, v73
	v_mul_f32_e32 v120, v93, v93
	v_pk_fma_f32 v[100:101], v[114:115], v[114:115], v[116:117]
	v_pk_add_f32 v[76:77], v[76:77], v[98:99]
	v_pk_mul_f32 v[122:123], v[74:75], v[74:75]
	v_pk_mul_f32 v[124:125], v[94:95], v[94:95]
	v_pk_fma_f32 v[118:119], v[72:73], v[72:73], v[118:119] op_sel_hi:[1,1,0]
	v_pk_fma_f32 v[120:121], v[92:93], v[92:93], v[120:121] op_sel_hi:[1,1,0]
	v_pk_add_f32 v[100:101], v[100:101], v[100:101] op_sel:[0,1] op_sel_hi:[1,0]
	v_pk_add_f32 v[76:77], v[76:77], v[76:77] op_sel:[0,1] op_sel_hi:[1,0]
	v_mov_b32_e32 v119, v124
	v_mov_b32_e32 v121, v125
	v_mov_b32_e32 v101, v123
	v_mov_b32_e32 v77, v122
	v_pk_add_f32 v[102:103], v[118:119], v[120:121]
	v_pk_add_f32 v[76:77], v[76:77], v[100:101]
	s_nop 0
	v_pk_add_f32 v[76:77], v[76:77], v[102:103]
	s_nop 0
	v_add_f32_e32 v61, v76, v77
	s_nop 0
	s_waitcnt lgkmcnt(0)
	s_nop 1
	v_add_f32_dpp v61, v61, v61 quad_perm:[1,0,3,2] row_mask:0xf bank_mask:0xf bound_ctrl:1
	s_nop 0
	s_waitcnt lgkmcnt(0)
	s_nop 1
	v_add_f32_dpp v61, v61, v61 quad_perm:[2,3,0,1] row_mask:0xf bank_mask:0xf bound_ctrl:1
	s_nop 0
	s_waitcnt lgkmcnt(0)
	s_nop 1
	v_add_f32_dpp v61, v61, v61 row_half_mirror row_mask:0xf bank_mask:0xf bound_ctrl:1
	s_nop 0
	s_waitcnt lgkmcnt(0)
	s_nop 1
	v_add_f32_dpp v61, v61, v61 row_mirror row_mask:0xf bank_mask:0xf bound_ctrl:1
	s_nop 0
	s_waitcnt lgkmcnt(0)
	s_nop 1
	v_add_f32_dpp v61, v61, v61 row_bcast:15 row_mask:0xa bank_mask:0xf
	s_nop 0
	s_waitcnt lgkmcnt(0)
; __device__ __forceinline__ float wave_max(float v) {
; #pragma unroll
;     for (int o = 1; o < 64; o <<= 1) v = fmaxf(v, __shfl_xor(v, o));
;     return v;
; }
;     ...
;             const float rstd = 1.0f / sqrtf(wave_sum(ss) * (1.0f / DM) + NORM_EPS);
;             if (F8 == 2) { unsigned* o4 = (unsigned*)((unsigned char*)xn + (size_t)row * DM) + lane; float mx = 0.f;
; #pragma unroll
;                 for (int q = 0; q < 8; ++q) { v[q] = v[q] * rstd * gn[q]; mx = fmaxf(fmaxf(mx, fmaxf(fabsf(v[q].x), fabsf(v[q].y))), fmaxf(fabsf(v[q].z), fabsf(v[q].w))); }
;                 mx = fmaxf(wave_max(mx), 1e-30f); const float qs = 127.0f / mx;
	s_nop 1
	v_add_f32_dpp v61, v61, v61 row_bcast:31 row_mask:0xc bank_mask:0xf
	s_nop 0
	v_readlane_b32 s98, v61, 63
	s_nop 1
	v_mov_b32_e32 v61, s98
	v_fmamk_f32 v61, v61, 0x3a000000, v58
	v_mul_f32_e32 v76, 0x4f800000, v61
	v_cmp_gt_f32_e32 vcc, s14, v61
	s_nop 1
	v_cndmask_b32_e32 v61, v61, v76, vcc
	v_sqrt_f32_e32 v76, v61
	s_nop 0
	v_add_u32_e32 v77, -1, v76
	v_add_u32_e32 v96, 1, v76
	v_fma_f32 v97, -v77, v76, v61
	v_fma_f32 v98, -v96, v76, v61
	v_cmp_ge_f32_e64 s[4:5], 0, v97
	s_nop 1
	v_cndmask_b32_e64 v76, v76, v77, s[4:5]
	v_cmp_lt_f32_e64 s[4:5], 0, v98
	s_nop 1
	v_cndmask_b32_e64 v76, v76, v96, s[4:5]
	v_mul_f32_e32 v77, 0x37800000, v76
	v_cndmask_b32_e32 v76, v76, v77, vcc
	v_cmp_class_f32_e32 vcc, v61, v59
	s_nop 1
	v_cndmask_b32_e32 v61, v76, v61, vcc
	v_div_scale_f32 v76, s[4:5], v61, v61, 1.0
	v_rcp_f32_e32 v77, v76
	v_div_scale_f32 v96, vcc, 1.0, v61, 1.0
	v_fma_f32 v97, -v76, v77, 1.0
	v_fmac_f32_e32 v77, v97, v77
	v_mul_f32_e32 v97, v96, v77
	v_fma_f32 v98, -v76, v97, v96
	v_fmac_f32_e32 v97, v98, v77
	v_fma_f32 v76, -v76, v97, v96
	v_div_fmas_f32 v76, v76, v77, v97
	v_div_fixup_f32 v76, v76, v61, 1.0
	v_pk_mul_f32 v[80:81], v[80:81], v[76:77] op_sel_hi:[1,0]
	v_pk_mul_f32 v[78:79], v[78:79], v[76:77] op_sel_hi:[1,0]
	v_pk_mul_f32 v[80:81], v[12:13], v[80:81]
	v_pk_mul_f32 v[62:63], v[62:63], v[76:77] op_sel_hi:[1,0]
	v_pk_mul_f32 v[82:83], v[82:83], v[76:77] op_sel_hi:[1,0]
	v_pk_mul_f32 v[64:65], v[64:65], v[76:77] op_sel_hi:[1,0]
	v_pk_mul_f32 v[84:85], v[84:85], v[76:77] op_sel_hi:[1,0]
	v_pk_mul_f32 v[66:67], v[66:67], v[76:77] op_sel_hi:[1,0]
	v_pk_mul_f32 v[86:87], v[86:87], v[76:77] op_sel_hi:[1,0]
	v_pk_mul_f32 v[78:79], v[10:11], v[78:79]
	v_max_f32_e64 v77, |v80|, |v81|
	v_pk_mul_f32 v[82:83], v[4:5], v[82:83]
	v_pk_mul_f32 v[62:63], v[2:3], v[62:63]
	v_max_f32_e64 v61, |v78|, |v79|
	v_pk_mul_f32 v[68:69], v[68:69], v[76:77] op_sel_hi:[1,0]
	v_pk_mul_f32 v[84:85], v[8:9], v[84:85]
	v_pk_mul_f32 v[64:65], v[6:7], v[64:65]
	v_max_f32_e64 v96, |v62|, |v63|
	v_max_f32_e64 v97, |v82|, |v83|
	v_max3_f32 v61, v61, 0, v77
	v_pk_mul_f32 v[68:69], v[18:19], v[68:69]
	v_pk_mul_f32 v[86:87], v[16:17], v[86:87]
	v_pk_mul_f32 v[66:67], v[14:15], v[66:67]
	v_max_f32_e64 v98, |v64|, |v65|
	v_max_f32_e64 v99, |v84|, |v85|
	v_max3_f32 v61, v61, v96, v97
	v_pk_mul_f32 v[88:89], v[88:89], v[76:77] op_sel_hi:[1,0]
	v_max_f32_e64 v77, |v68|, |v69|
	v_max_f32_e64 v100, |v66|, |v67|
	v_max_f32_e64 v101, |v86|, |v87|
	v_max3_f32 v61, v61, v98, v99
	v_pk_mul_f32 v[88:89], v[20:21], v[88:89]
	v_pk_mul_f32 v[70:71], v[70:71], v[76:77] op_sel_hi:[1,0]
	v_max3_f32 v61, v61, v100, v101
	v_max_f32_e64 v96, |v88|, |v89|
	v_pk_mul_f32 v[70:71], v[22:23], v[70:71]
	v_max3_f32 v61, v61, v77, v96
	v_pk_mul_f32 v[90:91], v[90:91], v[76:77] op_sel_hi:[1,0]
	v_max_f32_e64 v77, |v70|, |v71|
	v_pk_mul_f32 v[90:91], v[24:25], v[90:91]
	v_pk_mul_f32 v[72:73], v[72:73], v[76:77] op_sel_hi:[1,0]
	v_pk_mul_f32 v[92:93], v[92:93], v[76:77] op_sel_hi:[1,0]
	v_max_f32_e64 v96, |v90|, |v91|
	v_pk_mul_f32 v[92:93], v[28:29], v[92:93]
	v_pk_mul_f32 v[72:73], v[26:27], v[72:73]
	v_max3_f32 v61, v61, v77, v96
	v_max_f32_e64 v77, |v72|, |v73|
	v_max_f32_e64 v96, |v92|, |v93|
	v_max3_f32 v61, v61, v77, v96
	v_pk_mul_f32 v[74:75], v[74:75], v[76:77] op_sel_hi:[1,0]
	v_pk_mul_f32 v[76:77], v[94:95], v[76:77] op_sel_hi:[1,0]
	v_pk_mul_f32 v[74:75], v[30:31], v[74:75]
	v_pk_mul_f32 v[76:77], v[32:33], v[76:77]
	v_max_f32_e64 v94, |v74|, |v75|
	v_max_f32_e64 v95, |v76|, |v77|
	v_max3_f32 v61, v61, v94, v95
	s_nop 0
	s_waitcnt lgkmcnt(0)
	s_nop 0
	s_nop 1
	v_max_f32_dpp v61, v61, v61 quad_perm:[1,0,3,2] row_mask:0xf bank_mask:0xf bound_ctrl:1
	s_nop 0
	s_waitcnt lgkmcnt(0)
	s_nop 0
	s_nop 1
	v_max_f32_dpp v61, v61, v61 quad_perm:[2,3,0,1] row_mask:0xf bank_mask:0xf bound_ctrl:1
	s_nop 0
	s_waitcnt lgkmcnt(0)
	s_nop 0
	s_nop 1
	v_max_f32_dpp v61, v61, v61 row_half_mirror row_mask:0xf bank_mask:0xf bound_ctrl:1
	s_nop 0
	s_waitcnt lgkmcnt(0)
	s_nop 0
	s_nop 1
	v_max_f32_dpp v61, v61, v61 row_mirror row_mask:0xf bank_mask:0xf bound_ctrl:1
	s_nop 0
	s_waitcnt lgkmcnt(0)
	s_nop 0
	s_nop 1
	v_max_f32_dpp v61, v61, v61 row_bcast:15 row_mask:0xa bank_mask:0xf
	s_nop 0
	s_waitcnt lgkmcnt(0)
;     ...
;                 mx = fmaxf(wave_max(mx), 1e-30f); const float qs = 127.0f / mx;
; #pragma unroll
;                 for (int q = 0; q < 8; ++q) o4[64 * q] = pack_i8x4(v[q].x * qs, v[q].y * qs, v[q].z * qs, v[q].w * qs);
;                 if (lane == 0) ((float*)(ws + WS_ROWQ))[row] = mx * (1.0f / 127.0f); }
	s_nop 1
	v_max_f32_dpp v61, v61, v61 row_bcast:31 row_mask:0xc bank_mask:0xf
	s_nop 0
	v_readlane_b32 s98, v61, 63
	s_nop 1
	v_mov_b32_e32 v61, s98
	v_max_f32_e32 v61, s15, v61
	v_div_scale_f32 v96, s[4:5], v61, v61, s17
	v_rcp_f32_e32 v97, v96
	v_lshl_add_u64 v[94:95], s[6:7], 0, v[42:43]
	v_fma_f32 v98, -v96, v97, 1.0
	v_fmac_f32_e32 v97, v98, v97
	v_div_scale_f32 v98, vcc, s17, v61, s17
	v_mul_f32_e32 v99, v98, v97
	v_fma_f32 v100, -v96, v99, v98
	v_fmac_f32_e32 v99, v100, v97
	v_fma_f32 v96, -v96, v99, v98
	v_div_fmas_f32 v96, v96, v97, v99
	v_div_fixup_f32 v96, v96, v61, s17
	v_mul_f32_e32 v79, v79, v96
	v_mul_f32_e32 v78, v78, v96
	v_mul_f32_e32 v80, v80, v96
	v_mul_f32_e32 v81, v81, v96
	v_rndne_f32_e32 v79, v79
	v_rndne_f32_e32 v78, v78
	v_cvt_i32_f32_e32 v79, v79
	v_rndne_f32_e32 v80, v80
	v_rndne_f32_e32 v81, v81
	v_cvt_i32_f32_e32 v78, v78
	v_cvt_i32_f32_sdwa v80, v80 dst_sel:WORD_1 dst_unused:UNUSED_PAD src0_sel:DWORD
	v_cvt_i32_f32_e32 v81, v81
	v_lshlrev_b32_e32 v79, 8, v79
	v_and_b32_e32 v79, 0xff00, v79
	v_and_b32_e32 v80, 0xff0000, v80
	v_perm_b32 v78, v81, v78, s18
	v_or3_b32 v80, v78, v79, v80
	v_add_co_u32_e32 v78, vcc, s19, v94
	v_mul_f32_e32 v63, v63, v96
	s_nop 0
	v_addc_co_u32_e32 v79, vcc, 0, v95, vcc
	global_store_dword v[78:79], v80, off
	v_mul_f32_e32 v62, v62, v96
	v_mul_f32_e32 v80, v82, v96
	v_mul_f32_e32 v81, v83, v96
	v_rndne_f32_e32 v63, v63
	v_rndne_f32_e32 v62, v62
	v_cvt_i32_f32_e32 v63, v63
	v_rndne_f32_e32 v80, v80
	v_rndne_f32_e32 v81, v81
	v_cvt_i32_f32_e32 v62, v62
	v_cvt_i32_f32_sdwa v80, v80 dst_sel:WORD_1 dst_unused:UNUSED_PAD src0_sel:DWORD
	v_cvt_i32_f32_e32 v81, v81
	v_lshlrev_b32_e32 v63, 8, v63
	v_and_b32_e32 v63, 0xff00, v63
	v_and_b32_e32 v80, 0xff0000, v80
	v_perm_b32 v62, v81, v62, s18
	v_or3_b32 v62, v62, v63, v80
	v_mul_f32_e32 v63, v65, v96
	global_store_dword v[78:79], v62, off offset:256
	v_mul_f32_e32 v62, v64, v96
	v_mul_f32_e32 v64, v84, v96
	v_mul_f32_e32 v65, v85, v96
	v_rndne_f32_e32 v63, v63
	v_rndne_f32_e32 v62, v62
	v_cvt_i32_f32_e32 v63, v63
	v_rndne_f32_e32 v64, v64
	v_rndne_f32_e32 v65, v65
	v_cvt_i32_f32_e32 v62, v62
	v_cvt_i32_f32_sdwa v64, v64 dst_sel:WORD_1 dst_unused:UNUSED_PAD src0_sel:DWORD
	v_cvt_i32_f32_e32 v65, v65
	v_lshlrev_b32_e32 v63, 8, v63
	v_and_b32_e32 v63, 0xff00, v63
	v_and_b32_e32 v64, 0xff0000, v64
	v_perm_b32 v62, v65, v62, s18
	v_or3_b32 v62, v62, v63, v64
	v_mul_f32_e32 v63, v67, v96
	global_store_dword v[78:79], v62, off offset:512
	v_mul_f32_e32 v62, v66, v96
	v_mul_f32_e32 v64, v86, v96
	v_mul_f32_e32 v65, v87, v96
	v_rndne_f32_e32 v63, v63
	v_rndne_f32_e32 v62, v62
	v_cvt_i32_f32_e32 v63, v63
	v_rndne_f32_e32 v64, v64
	v_rndne_f32_e32 v65, v65
	v_cvt_i32_f32_e32 v62, v62
	v_cvt_i32_f32_sdwa v64, v64 dst_sel:WORD_1 dst_unused:UNUSED_PAD src0_sel:DWORD
	v_cvt_i32_f32_e32 v65, v65
	v_lshlrev_b32_e32 v63, 8, v63
	v_and_b32_e32 v63, 0xff00, v63
	v_and_b32_e32 v64, 0xff0000, v64
	v_perm_b32 v62, v65, v62, s18
	v_or3_b32 v62, v62, v63, v64
	v_mul_f32_e32 v63, v69, v96
	global_store_dword v[78:79], v62, off offset:768
	v_mul_f32_e32 v62, v68, v96
	v_mul_f32_e32 v64, v88, v96
	v_mul_f32_e32 v65, v89, v96
	v_rndne_f32_e32 v63, v63
	v_rndne_f32_e32 v62, v62
	v_cvt_i32_f32_e32 v63, v63
	v_rndne_f32_e32 v64, v64
	v_rndne_f32_e32 v65, v65
	v_cvt_i32_f32_e32 v62, v62
	v_cvt_i32_f32_sdwa v64, v64 dst_sel:WORD_1 dst_unused:UNUSED_PAD src0_sel:DWORD
	v_cvt_i32_f32_e32 v65, v65
	v_lshlrev_b32_e32 v63, 8, v63
	v_and_b32_e32 v63, 0xff00, v63
	v_and_b32_e32 v64, 0xff0000, v64
	v_perm_b32 v62, v65, v62, s18
	v_or3_b32 v62, v62, v63, v64
	v_mul_f32_e32 v63, v71, v96
	global_store_dword v[78:79], v62, off offset:1024
	v_mul_f32_e32 v62, v70, v96
	v_mul_f32_e32 v64, v90, v96
	v_mul_f32_e32 v65, v91, v96
	v_rndne_f32_e32 v63, v63
	v_rndne_f32_e32 v62, v62
	v_cvt_i32_f32_e32 v63, v63
	v_rndne_f32_e32 v64, v64
	v_rndne_f32_e32 v65, v65
	v_cvt_i32_f32_e32 v62, v62
	v_cvt_i32_f32_sdwa v64, v64 dst_sel:WORD_1 dst_unused:UNUSED_PAD src0_sel:DWORD
	v_cvt_i32_f32_e32 v65, v65
	v_lshlrev_b32_e32 v63, 8, v63
	v_and_b32_e32 v63, 0xff00, v63
	v_and_b32_e32 v64, 0xff0000, v64
	v_perm_b32 v62, v65, v62, s18
	v_or3_b32 v62, v62, v63, v64
	v_mul_f32_e32 v63, v73, v96
	global_store_dword v[78:79], v62, off offset:1280
	v_mul_f32_e32 v62, v72, v96
	v_mul_f32_e32 v64, v92, v96
	v_mul_f32_e32 v65, v93, v96
	v_rndne_f32_e32 v63, v63
	v_rndne_f32_e32 v62, v62
	v_cvt_i32_f32_e32 v63, v63
	v_rndne_f32_e32 v64, v64
	v_rndne_f32_e32 v65, v65
	v_cvt_i32_f32_e32 v62, v62
	v_cvt_i32_f32_sdwa v64, v64 dst_sel:WORD_1 dst_unused:UNUSED_PAD src0_sel:DWORD
	v_cvt_i32_f32_e32 v65, v65
	v_lshlrev_b32_e32 v63, 8, v63
	v_and_b32_e32 v63, 0xff00, v63
	v_and_b32_e32 v64, 0xff0000, v64
	v_perm_b32 v62, v65, v62, s18
	v_or3_b32 v62, v62, v63, v64
	v_mul_f32_e32 v63, v75, v96
	global_store_dword v[78:79], v62, off offset:1536
	v_mul_f32_e32 v62, v74, v96
	v_mul_f32_e32 v64, v76, v96
	v_mul_f32_e32 v65, v77, v96
	v_rndne_f32_e32 v63, v63
	v_rndne_f32_e32 v62, v62
	v_cvt_i32_f32_e32 v63, v63
	v_rndne_f32_e32 v64, v64
	v_rndne_f32_e32 v65, v65
	v_cvt_i32_f32_e32 v62, v62
	v_cvt_i32_f32_sdwa v64, v64 dst_sel:WORD_1 dst_unused:UNUSED_PAD src0_sel:DWORD
	v_cvt_i32_f32_e32 v65, v65
	v_lshlrev_b32_e32 v63, 8, v63
	v_and_b32_e32 v63, 0xff00, v63
	v_and_b32_e32 v64, 0xff0000, v64
	v_perm_b32 v62, v65, v62, s18
	v_or3_b32 v62, v62, v63, v64
	global_store_dword v[78:79], v62, off offset:1792
	s_and_saveexec_b64 s[4:5], s[0:1]
	s_cbranch_execz .LBB0_1336
	v_lshl_add_u64 v[62:63], s[6:7], 0, v[50:51]
	v_mul_f32_e32 v61, 0x3c010204, v61
	v_readfirstlane_b32 s22, v62
	v_readfirstlane_b32 s23, v63
	s_nop 4
	global_store_dword v60, v61, s[22:23]

; template <bool SB> __device__ __forceinline__ void load_row(const void* xin, size_t row, int lane, f32x4 (&v)[8]) {
;     if (SB) { typedef _Float16 h16x4_t __attribute__((ext_vector_type(4))); const h16x4_t* xr = (const h16x4_t*)((const bf16*)xin + row * DM) + lane;
; #pragma unroll
;         for (int q = 0; q < 8; ++q) { const h16x4_t w = xr[64 * q]; v[q] = (f32x4){(float)w[0], (float)w[1], (float)w[2], (float)w[3]}; } }
;     ...
;         for (int blk = gw; blk < MTOK / 16; blk += NGW) {
;             const int row0 = blk * 16; f32x4 prev[8];
;             if ((row0 % SEQ) == 0) {
; #pragma unroll
;                 for (int q = 0; q < 8; ++q) prev[q] = (f32x4){0.f, 0.f, 0.f, 0.f};
;             } else {
;                 float ss = 0.f; load_row<SB>(xin, (size_t)(row0 - 1), lane, prev);
; #pragma unroll
;                 for (int q = 0; q < 8; ++q) ss += (prev[q].x * prev[q].x + prev[q].y * prev[q].y) + (prev[q].z * prev[q].z + prev[q].w * prev[q].w);
;                 const float rstd = 1.0f / sqrtf(wave_sum(ss) * (1.0f / DM) + NORM_EPS);
.LBB0_2195:
	s_lshl_b32 s2, s8, 4
	s_and_b32 s0, s8, 0xff
	s_cmp_lg_u32 s0, 0
	s_cbranch_scc0 .LBB0_2197
	s_ashr_i32 s3, s2, 31
	s_lshl_b64 s[0:1], s[2:3], 12
	v_lshl_add_u64 v[36:37], v[68:69], 0, s[0:1]
	global_load_dwordx2 v[38:39], v[36:37], off offset:-4096
	global_load_dwordx2 v[40:41], v[36:37], off offset:-3584
	global_load_dwordx2 v[42:43], v[36:37], off offset:-3072
	global_load_dwordx2 v[44:45], v[36:37], off offset:-2560
	global_load_dwordx2 v[46:47], v[36:37], off offset:-2048
	global_load_dwordx2 v[48:49], v[36:37], off offset:-1536
	global_load_dwordx2 v[50:51], v[36:37], off offset:-1024
	global_load_dwordx2 v[52:53], v[36:37], off offset:-512
	s_waitcnt vmcnt(7)
	v_cvt_f32_f16_e32 v36, v38
	v_cvt_f32_f16_sdwa v37, v38 dst_sel:DWORD dst_unused:UNUSED_PAD src0_sel:WORD_1
	v_cvt_f32_f16_e32 v38, v39
	v_cvt_f32_f16_sdwa v39, v39 dst_sel:DWORD dst_unused:UNUSED_PAD src0_sel:WORD_1
	s_waitcnt vmcnt(6)
	v_cvt_f32_f16_e32 v54, v40
	v_cvt_f32_f16_sdwa v55, v40 dst_sel:DWORD dst_unused:UNUSED_PAD src0_sel:WORD_1
	v_cvt_f32_f16_e32 v40, v41
	v_cvt_f32_f16_sdwa v41, v41 dst_sel:DWORD dst_unused:UNUSED_PAD src0_sel:WORD_1
	s_waitcnt vmcnt(5)
	v_cvt_f32_f16_e32 v56, v42
	v_cvt_f32_f16_sdwa v57, v42 dst_sel:DWORD dst_unused:UNUSED_PAD src0_sel:WORD_1
	v_cvt_f32_f16_e32 v42, v43
	v_cvt_f32_f16_sdwa v43, v43 dst_sel:DWORD dst_unused:UNUSED_PAD src0_sel:WORD_1
	s_waitcnt vmcnt(4)
	v_cvt_f32_f16_e32 v58, v44
	v_cvt_f32_f16_sdwa v59, v44 dst_sel:DWORD dst_unused:UNUSED_PAD src0_sel:WORD_1
	v_cvt_f32_f16_e32 v44, v45
	v_cvt_f32_f16_sdwa v45, v45 dst_sel:DWORD dst_unused:UNUSED_PAD src0_sel:WORD_1
	s_waitcnt vmcnt(3)
	v_cvt_f32_f16_e32 v60, v46
	v_cvt_f32_f16_sdwa v61, v46 dst_sel:DWORD dst_unused:UNUSED_PAD src0_sel:WORD_1
	v_cvt_f32_f16_e32 v46, v47
	v_cvt_f32_f16_sdwa v47, v47 dst_sel:DWORD dst_unused:UNUSED_PAD src0_sel:WORD_1
	s_waitcnt vmcnt(0)
	v_cvt_f32_f16_e32 v72, v52
	v_cvt_f32_f16_sdwa v73, v52 dst_sel:DWORD dst_unused:UNUSED_PAD src0_sel:WORD_1
	v_cvt_f32_f16_e32 v74, v53
	v_cvt_f32_f16_sdwa v75, v53 dst_sel:DWORD dst_unused:UNUSED_PAD src0_sel:WORD_1
	v_mov_b32_e32 v52, v37
	v_mov_b32_e32 v53, v55
	v_mov_b32_e32 v78, v39
	v_mov_b32_e32 v79, v41
	v_cvt_f32_f16_e32 v62, v48
	v_cvt_f32_f16_sdwa v63, v48 dst_sel:DWORD dst_unused:UNUSED_PAD src0_sel:WORD_1
	v_cvt_f32_f16_e32 v48, v49
	v_cvt_f32_f16_sdwa v49, v49 dst_sel:DWORD dst_unused:UNUSED_PAD src0_sel:WORD_1
	v_cvt_f32_f16_e32 v64, v50
	v_cvt_f32_f16_sdwa v65, v50 dst_sel:DWORD dst_unused:UNUSED_PAD src0_sel:WORD_1
	v_cvt_f32_f16_e32 v66, v51
	v_cvt_f32_f16_sdwa v67, v51 dst_sel:DWORD dst_unused:UNUSED_PAD src0_sel:WORD_1
	v_mov_b32_e32 v50, v36
	v_mov_b32_e32 v51, v54
	v_mov_b32_e32 v76, v38
	v_mov_b32_e32 v77, v40
	v_mov_b32_e32 v82, v57
	v_mov_b32_e32 v83, v43
	v_pk_mul_f32 v[52:53], v[52:53], v[52:53]
	v_pk_mul_f32 v[78:79], v[78:79], v[78:79]
	v_mov_b32_e32 v80, v56
	v_mov_b32_e32 v81, v42
	v_pk_mul_f32 v[82:83], v[82:83], v[82:83]
	v_pk_fma_f32 v[50:51], v[50:51], v[50:51], v[52:53]
	v_pk_fma_f32 v[52:53], v[76:77], v[76:77], v[78:79]
	v_mul_f32_e32 v84, v59, v59
	v_mul_f32_e32 v86, v45, v45
	v_pk_fma_f32 v[76:77], v[80:81], v[80:81], v[82:83]
	v_pk_add_f32 v[50:51], v[50:51], v[52:53]
	v_pk_mul_f32 v[88:89], v[60:61], v[60:61]
	v_pk_mul_f32 v[90:91], v[46:47], v[46:47]
	v_pk_fma_f32 v[84:85], v[58:59], v[58:59], v[84:85] op_sel_hi:[1,1,0]
	v_pk_fma_f32 v[86:87], v[44:45], v[44:45], v[86:87] op_sel_hi:[1,1,0]
	v_pk_add_f32 v[52:53], v[76:77], v[76:77] op_sel:[0,1] op_sel_hi:[1,0]
	v_pk_add_f32 v[50:51], v[50:51], v[50:51] op_sel:[0,1] op_sel_hi:[1,0]
	v_mov_b32_e32 v94, v63
	v_mov_b32_e32 v95, v49
	v_mov_b32_e32 v85, v90
	v_mov_b32_e32 v87, v91
	v_mov_b32_e32 v53, v89
	v_mov_b32_e32 v51, v88
	v_mov_b32_e32 v92, v62
	v_mov_b32_e32 v93, v48
	v_pk_mul_f32 v[94:95], v[94:95], v[94:95]
	v_pk_add_f32 v[76:77], v[84:85], v[86:87]
	v_pk_add_f32 v[50:51], v[50:51], v[52:53]
	v_mul_f32_e32 v96, v65, v65
	v_mul_f32_e32 v98, v67, v67
	v_pk_fma_f32 v[78:79], v[92:93], v[92:93], v[94:95]
	v_pk_add_f32 v[50:51], v[50:51], v[76:77]
	v_pk_mul_f32 v[100:101], v[72:73], v[72:73]
	v_pk_mul_f32 v[102:103], v[74:75], v[74:75]
	v_pk_fma_f32 v[96:97], v[64:65], v[64:65], v[96:97] op_sel_hi:[1,1,0]
	v_pk_fma_f32 v[98:99], v[66:67], v[66:67], v[98:99] op_sel_hi:[1,1,0]
	v_pk_add_f32 v[78:79], v[78:79], v[78:79] op_sel:[0,1] op_sel_hi:[1,0]
	v_pk_add_f32 v[50:51], v[50:51], v[50:51] op_sel:[0,1] op_sel_hi:[1,0]
	v_mov_b32_e32 v97, v102
	v_mov_b32_e32 v99, v103
	v_mov_b32_e32 v79, v101
	v_mov_b32_e32 v51, v100
	v_pk_add_f32 v[80:81], v[96:97], v[98:99]
	v_pk_add_f32 v[50:51], v[50:51], v[78:79]
	s_nop 0
	v_pk_add_f32 v[50:51], v[50:51], v[80:81]
	s_nop 0
	v_add_f32_e32 v35, v50, v51
	s_nop 0
	s_waitcnt lgkmcnt(0)
; __device__ __forceinline__ float wave_sum(float v) {
; #pragma unroll
;     for (int o = 1; o < 64; o <<= 1) v += __shfl_xor(v, o);
;     return v;
; }
;     ...
;                 const float rstd = 1.0f / sqrtf(wave_sum(ss) * (1.0f / DM) + NORM_EPS);
; #pragma unroll
;                 for (int q = 0; q < 8; ++q) prev[q] = prev[q] * rstd * gn[q];
	s_nop 1
	v_add_f32_dpp v35, v35, v35 quad_perm:[1,0,3,2] row_mask:0xf bank_mask:0xf bound_ctrl:1
	s_nop 0
	s_waitcnt lgkmcnt(0)
	s_nop 1
	v_add_f32_dpp v35, v35, v35 quad_perm:[2,3,0,1] row_mask:0xf bank_mask:0xf bound_ctrl:1
	s_nop 0
	s_waitcnt lgkmcnt(0)
	s_nop 1
	v_add_f32_dpp v35, v35, v35 row_half_mirror row_mask:0xf bank_mask:0xf bound_ctrl:1
	s_nop 0
	s_waitcnt lgkmcnt(0)
	s_nop 1
	v_add_f32_dpp v35, v35, v35 row_mirror row_mask:0xf bank_mask:0xf bound_ctrl:1
	s_nop 0
	s_waitcnt lgkmcnt(0)
	s_nop 1
	v_add_f32_dpp v35, v35, v35 row_bcast:15 row_mask:0xa bank_mask:0xf
	s_nop 0
	s_waitcnt lgkmcnt(0)
	s_nop 1
	v_add_f32_dpp v35, v35, v35 row_bcast:31 row_mask:0xc bank_mask:0xf
	s_nop 0
	v_readlane_b32 s98, v35, 63
	s_nop 1
	v_mov_b32_e32 v35, s98
	v_fmamk_f32 v35, v35, 0x3a000000, v112
	v_mul_f32_e32 v50, 0x4f800000, v35
	v_cmp_gt_f32_e32 vcc, s12, v35
	s_nop 1
	v_cndmask_b32_e32 v35, v35, v50, vcc
	v_sqrt_f32_e32 v50, v35
	s_nop 0
	v_add_u32_e32 v51, -1, v50
	v_add_u32_e32 v52, 1, v50
	v_fma_f32 v53, -v51, v50, v35
	v_fma_f32 v76, -v52, v50, v35
	v_cmp_ge_f32_e64 s[0:1], 0, v53
	s_nop 1
	v_cndmask_b32_e64 v50, v50, v51, s[0:1]
	v_cmp_lt_f32_e64 s[0:1], 0, v76
	s_nop 1
	v_cndmask_b32_e64 v50, v50, v52, s[0:1]
	v_mul_f32_e32 v51, 0x37800000, v50
	v_cndmask_b32_e32 v50, v50, v51, vcc
	v_cmp_class_f32_e32 vcc, v35, v113
	s_nop 1
	v_cndmask_b32_e32 v35, v50, v35, vcc
	v_div_scale_f32 v50, s[0:1], v35, v35, 1.0
	v_rcp_f32_e32 v51, v50
	v_div_scale_f32 v52, vcc, 1.0, v35, 1.0
	v_fma_f32 v53, -v50, v51, 1.0
	v_fmac_f32_e32 v51, v53, v51
	v_mul_f32_e32 v53, v52, v51
	v_fma_f32 v76, -v50, v53, v52
	v_fmac_f32_e32 v53, v76, v51
	v_fma_f32 v50, -v50, v53, v52
	v_div_fmas_f32 v50, v50, v51, v53
	v_div_fixup_f32 v76, v50, v35, 1.0
	v_pk_mul_f32 v[52:53], v[56:57], v[76:77] op_sel_hi:[1,0]
	v_pk_mul_f32 v[56:57], v[58:59], v[76:77] op_sel_hi:[1,0]
	v_pk_mul_f32 v[60:61], v[60:61], v[76:77] op_sel_hi:[1,0]
	v_pk_mul_f32 v[62:63], v[62:63], v[76:77] op_sel_hi:[1,0]
	v_pk_mul_f32 v[36:37], v[36:37], v[76:77] op_sel_hi:[1,0]
	v_pk_mul_f32 v[38:39], v[38:39], v[76:77] op_sel_hi:[1,0]
	v_pk_mul_f32 v[50:51], v[54:55], v[76:77] op_sel_hi:[1,0]
	v_pk_mul_f32 v[40:41], v[40:41], v[76:77] op_sel_hi:[1,0]
	v_pk_mul_f32 v[54:55], v[42:43], v[76:77] op_sel_hi:[1,0]
	v_pk_mul_f32 v[58:59], v[44:45], v[76:77] op_sel_hi:[1,0]
	v_pk_mul_f32 v[78:79], v[46:47], v[76:77] op_sel_hi:[1,0]
	v_pk_mul_f32 v[80:81], v[48:49], v[76:77] op_sel_hi:[1,0]
	v_pk_mul_f32 v[44:45], v[6:7], v[52:53]
	v_pk_mul_f32 v[48:49], v[14:15], v[56:57]
	v_pk_mul_f32 v[52:53], v[18:19], v[60:61]
	v_pk_mul_f32 v[56:57], v[22:23], v[62:63]
	v_pk_mul_f32 v[60:61], v[64:65], v[76:77] op_sel_hi:[1,0]
	v_pk_mul_f32 v[62:63], v[66:67], v[76:77] op_sel_hi:[1,0]
	v_pk_mul_f32 v[64:65], v[72:73], v[76:77] op_sel_hi:[1,0]
	v_pk_mul_f32 v[66:67], v[74:75], v[76:77] op_sel_hi:[1,0]
	v_pk_mul_f32 v[38:39], v[12:13], v[38:39]
	v_pk_mul_f32 v[36:37], v[10:11], v[36:37]
	v_pk_mul_f32 v[42:43], v[4:5], v[40:41]
	v_pk_mul_f32 v[40:41], v[2:3], v[50:51]
	v_pk_mul_f32 v[46:47], v[8:9], v[54:55]
	v_pk_mul_f32 v[50:51], v[16:17], v[58:59]
	v_pk_mul_f32 v[54:55], v[20:21], v[78:79]
	v_pk_mul_f32 v[58:59], v[24:25], v[80:81]
	v_pk_mul_f32 v[62:63], v[28:29], v[62:63]
	v_pk_mul_f32 v[60:61], v[26:27], v[60:61]
	v_pk_mul_f32 v[66:67], v[32:33], v[66:67]
	v_pk_mul_f32 v[64:65], v[30:31], v[64:65]
	s_branch .LBB0_2198

; #define LAS __attribute__((address_space(3)))
;     ...
;             for (int rr = 0; rr < 16; ++rr) {
;                 const int row = row0 + rr; f32x4 v[8]; float ss = 0.f; load_row<SB>(xin, (size_t)row, lane, v);
; #pragma unroll
;                 for (int q = 0; q < 8; ++q) ss += (v[q].x * v[q].x + v[q].y * v[q].y) + (v[q].z * v[q].z + v[q].w * v[q].w);
;                 const float rstd = 1.0f / sqrtf(wave_sum(ss) * (1.0f / DM) + NORM_EPS);
;     ...
;                     for (int q = 0; q < 8; ++q) { const f32x4 mx = *(const LAS f32x4*)(mixs + z * DM + 4 * lane + 256 * q); const f32x4 y = v[q] + (prev[q] - v[q]) * mx;
.LBB0_2199:
	s_or_b32 s0, s3, s2
	s_ashr_i32 s1, s0, 31
	s_lshl_b64 s[0:1], s[0:1], 12
	v_lshl_add_u64 v[72:73], v[68:69], 0, s[0:1]
	global_load_dwordx2 v[74:75], v[72:73], off
	global_load_dwordx2 v[76:77], v[72:73], off offset:512
	global_load_dwordx2 v[78:79], v[72:73], off offset:1024
	global_load_dwordx2 v[80:81], v[72:73], off offset:1536
	global_load_dwordx2 v[82:83], v[72:73], off offset:2048
	global_load_dwordx2 v[84:85], v[72:73], off offset:2560
	global_load_dwordx2 v[86:87], v[72:73], off offset:3072
	global_load_dwordx2 v[88:89], v[72:73], off offset:3584
	s_waitcnt vmcnt(13)
	v_xor_b32_e32 v147, 0x80000000, v13
	v_xor_b32_e32 v146, 0x80000000, v12
	s_ashr_i32 s7, s6, 31
	s_lshl_b64 s[16:17], s[6:7], 12
	s_waitcnt vmcnt(7)
	v_cvt_f32_f16_e32 v104, v74
	v_cvt_f32_f16_sdwa v105, v74 dst_sel:DWORD dst_unused:UNUSED_PAD src0_sel:WORD_1
	v_cvt_f32_f16_e32 v74, v75
	v_cvt_f32_f16_sdwa v75, v75 dst_sel:DWORD dst_unused:UNUSED_PAD src0_sel:WORD_1
	s_waitcnt vmcnt(6)
	v_cvt_f32_f16_sdwa v119, v76 dst_sel:DWORD dst_unused:UNUSED_PAD src0_sel:WORD_1
	v_cvt_f32_f16_sdwa v121, v77 dst_sel:DWORD dst_unused:UNUSED_PAD src0_sel:WORD_1
	v_cvt_f32_f16_e32 v118, v76
	v_cvt_f32_f16_e32 v120, v77
	s_waitcnt vmcnt(5)
	v_cvt_f32_f16_sdwa v123, v78 dst_sel:DWORD dst_unused:UNUSED_PAD src0_sel:WORD_1
	v_cvt_f32_f16_sdwa v125, v79 dst_sel:DWORD dst_unused:UNUSED_PAD src0_sel:WORD_1
	v_cvt_f32_f16_e32 v122, v78
	v_cvt_f32_f16_e32 v124, v79
	s_waitcnt vmcnt(4)
	v_cvt_f32_f16_sdwa v127, v80 dst_sel:DWORD dst_unused:UNUSED_PAD src0_sel:WORD_1
	v_cvt_f32_f16_sdwa v129, v81 dst_sel:DWORD dst_unused:UNUSED_PAD src0_sel:WORD_1
	v_cvt_f32_f16_e32 v126, v80
	v_cvt_f32_f16_e32 v128, v81
	s_waitcnt vmcnt(3)
	v_cvt_f32_f16_e32 v130, v82
	v_cvt_f32_f16_sdwa v131, v82 dst_sel:DWORD dst_unused:UNUSED_PAD src0_sel:WORD_1
	v_cvt_f32_f16_e32 v132, v83
	v_cvt_f32_f16_sdwa v133, v83 dst_sel:DWORD dst_unused:UNUSED_PAD src0_sel:WORD_1
	v_mov_b32_e32 v76, v105
	v_mov_b32_e32 v77, v119
	v_mov_b32_e32 v80, v75
	v_mov_b32_e32 v81, v121
	s_waitcnt vmcnt(2)
	v_cvt_f32_f16_e32 v134, v84
	v_cvt_f32_f16_sdwa v135, v84 dst_sel:DWORD dst_unused:UNUSED_PAD src0_sel:WORD_1
	v_cvt_f32_f16_e32 v136, v85
	v_cvt_f32_f16_sdwa v137, v85 dst_sel:DWORD dst_unused:UNUSED_PAD src0_sel:WORD_1
	v_mov_b32_e32 v72, v104
	v_mov_b32_e32 v73, v118
	v_mov_b32_e32 v78, v74
	v_mov_b32_e32 v79, v120
	v_mov_b32_e32 v84, v123
	v_mov_b32_e32 v85, v125
	v_pk_mul_f32 v[76:77], v[76:77], v[76:77]
	v_pk_mul_f32 v[80:81], v[80:81], v[80:81]
	v_mov_b32_e32 v82, v122
	v_mov_b32_e32 v83, v124
	v_pk_mul_f32 v[84:85], v[84:85], v[84:85]
	v_pk_fma_f32 v[72:73], v[72:73], v[72:73], v[76:77]
	v_pk_fma_f32 v[76:77], v[78:79], v[78:79], v[80:81]
	s_waitcnt vmcnt(1)
	v_cvt_f32_f16_e32 v138, v86
	v_cvt_f32_f16_sdwa v139, v86 dst_sel:DWORD dst_unused:UNUSED_PAD src0_sel:WORD_1
	v_cvt_f32_f16_sdwa v141, v87 dst_sel:DWORD dst_unused:UNUSED_PAD src0_sel:WORD_1
	s_waitcnt vmcnt(0)
	v_cvt_f32_f16_e32 v142, v88
	v_cvt_f32_f16_sdwa v143, v88 dst_sel:DWORD dst_unused:UNUSED_PAD src0_sel:WORD_1
	v_mul_f32_e32 v86, v127, v127
	v_mul_f32_e32 v88, v129, v129
	v_pk_fma_f32 v[78:79], v[82:83], v[82:83], v[84:85]
	v_pk_add_f32 v[72:73], v[72:73], v[76:77]
	v_cvt_f32_f16_e32 v140, v87
	v_cvt_f32_f16_e32 v144, v89
	v_cvt_f32_f16_sdwa v145, v89 dst_sel:DWORD dst_unused:UNUSED_PAD src0_sel:WORD_1
	v_pk_mul_f32 v[90:91], v[130:131], v[130:131]
	v_pk_mul_f32 v[92:93], v[132:133], v[132:133]
	v_pk_fma_f32 v[86:87], v[126:127], v[126:127], v[86:87] op_sel_hi:[1,1,0]
	v_pk_fma_f32 v[88:89], v[128:129], v[128:129], v[88:89] op_sel_hi:[1,1,0]
	v_pk_add_f32 v[76:77], v[78:79], v[78:79] op_sel:[0,1] op_sel_hi:[1,0]
	v_pk_add_f32 v[72:73], v[72:73], v[72:73] op_sel:[0,1] op_sel_hi:[1,0]
	v_mov_b32_e32 v96, v135
	v_mov_b32_e32 v97, v137
	v_mov_b32_e32 v87, v92
	v_mov_b32_e32 v89, v93
	v_mov_b32_e32 v77, v91
	v_mov_b32_e32 v73, v90
	v_mov_b32_e32 v94, v134
	v_mov_b32_e32 v95, v136
	v_pk_mul_f32 v[96:97], v[96:97], v[96:97]
	v_pk_add_f32 v[78:79], v[86:87], v[88:89]
	v_pk_add_f32 v[72:73], v[72:73], v[76:77]
	v_mul_f32_e32 v98, v139, v139
	v_mul_f32_e32 v100, v141, v141
	v_pk_fma_f32 v[80:81], v[94:95], v[94:95], v[96:97]
	v_pk_add_f32 v[72:73], v[72:73], v[78:79]
	v_pk_mul_f32 v[102:103], v[142:143], v[142:143]
	v_pk_mul_f32 v[114:115], v[144:145], v[144:145]
	v_pk_fma_f32 v[98:99], v[138:139], v[138:139], v[98:99] op_sel_hi:[1,1,0]
	v_pk_fma_f32 v[100:101], v[140:141], v[140:141], v[100:101] op_sel_hi:[1,1,0]
	v_pk_add_f32 v[80:81], v[80:81], v[80:81] op_sel:[0,1] op_sel_hi:[1,0]
	v_pk_add_f32 v[72:73], v[72:73], v[72:73] op_sel:[0,1] op_sel_hi:[1,0]
	v_mov_b32_e32 v99, v114
	v_mov_b32_e32 v101, v115
	v_mov_b32_e32 v81, v103
	v_mov_b32_e32 v73, v102
	v_pk_add_f32 v[82:83], v[98:99], v[100:101]
	v_pk_add_f32 v[72:73], v[72:73], v[80:81]
	v_mov_b64_e32 v[78:79], v[38:39]
	v_pk_add_f32 v[72:73], v[72:73], v[82:83]
	v_mov_b64_e32 v[76:77], v[36:37]
	v_add_f32_e32 v35, v72, v73
	s_nop 0
	v_mov_b64_e32 v[82:83], v[42:43]
	v_mov_b64_e32 v[80:81], v[40:41]
	v_mov_b64_e32 v[116:117], v[66:67]
	v_mov_b64_e32 v[114:115], v[64:65]
	s_waitcnt lgkmcnt(0)
	s_nop 1
	v_add_f32_dpp v35, v35, v35 quad_perm:[1,0,3,2] row_mask:0xf bank_mask:0xf bound_ctrl:1
	s_nop 0
	v_mov_b64_e32 v[86:87], v[46:47]
	v_mov_b64_e32 v[90:91], v[50:51]
	v_mov_b64_e32 v[94:95], v[54:55]
	v_mov_b64_e32 v[98:99], v[58:59]
	s_waitcnt lgkmcnt(0)
; #define LAS __attribute__((address_space(3)))
;     ...
;                 const float rstd = 1.0f / sqrtf(wave_sum(ss) * (1.0f / DM) + NORM_EPS);
; #pragma unroll
;                 for (int q = 0; q < 8; ++q) v[q] = v[q] * rstd * gn[q];
; #pragma unroll 1
;                 for (int z = 0; z < 6; ++z) { v2u* o8 = (v2u*)(xm + ((size_t)z * MTOK + row) * DM) + lane;
; #pragma unroll
;                     for (int q = 0; q < 8; ++q) { const f32x4 mx = *(const LAS f32x4*)(mixs + z * DM + 4 * lane + 256 * q); const f32x4 y = v[q] + (prev[q] - v[q]) * mx;
	s_nop 1
	v_add_f32_dpp v35, v35, v35 quad_perm:[2,3,0,1] row_mask:0xf bank_mask:0xf bound_ctrl:1
	s_nop 0
	v_mov_b64_e32 v[102:103], v[62:63]
	v_mov_b64_e32 v[84:85], v[44:45]
	v_mov_b64_e32 v[88:89], v[48:49]
	v_mov_b64_e32 v[92:93], v[52:53]
	s_waitcnt lgkmcnt(0)
	s_nop 1
	v_add_f32_dpp v35, v35, v35 row_half_mirror row_mask:0xf bank_mask:0xf bound_ctrl:1
	s_nop 0
	v_mov_b64_e32 v[96:97], v[56:57]
	v_mov_b64_e32 v[100:101], v[60:61]
	s_waitcnt lgkmcnt(0)
	s_nop 1
	v_add_f32_dpp v35, v35, v35 row_mirror row_mask:0xf bank_mask:0xf bound_ctrl:1
	s_nop 0
	s_waitcnt lgkmcnt(0)
	s_nop 1
	v_add_f32_dpp v35, v35, v35 row_bcast:15 row_mask:0xa bank_mask:0xf
	s_nop 0
	v_lshl_add_u64 v[72:73], v[70:71], 0, s[16:17]
	s_waitcnt lgkmcnt(0)
	s_nop 1
	v_add_f32_dpp v35, v35, v35 row_bcast:31 row_mask:0xc bank_mask:0xf
	s_nop 0
	v_readlane_b32 s98, v35, 63
	s_nop 1
	v_mov_b32_e32 v35, s98
	v_fmamk_f32 v35, v35, 0x3a000000, v112
	v_mul_f32_e32 v36, 0x4f800000, v35
	v_cmp_gt_f32_e32 vcc, s12, v35
	s_nop 1
	v_cndmask_b32_e32 v35, v35, v36, vcc
	v_sqrt_f32_e32 v36, v35
	s_nop 0
	v_add_u32_e32 v37, -1, v36
	v_add_u32_e32 v38, 1, v36
	v_fma_f32 v39, -v37, v36, v35
	v_fma_f32 v40, -v38, v36, v35
	v_cmp_ge_f32_e64 s[0:1], 0, v39
	s_nop 1
	v_cndmask_b32_e64 v36, v36, v37, s[0:1]
	v_cmp_lt_f32_e64 s[0:1], 0, v40
	s_nop 1
	v_cndmask_b32_e64 v36, v36, v38, s[0:1]
	v_mul_f32_e32 v37, 0x37800000, v36
	v_cndmask_b32_e32 v36, v36, v37, vcc
	v_cmp_class_f32_e32 vcc, v35, v113
	s_nop 1
	v_cndmask_b32_e32 v35, v36, v35, vcc
	v_div_scale_f32 v36, s[0:1], v35, v35, 1.0
	v_rcp_f32_e32 v37, v36
	v_div_scale_f32 v38, vcc, 1.0, v35, 1.0
	s_mov_b64 s[0:1], 0
	v_fma_f32 v39, -v36, v37, 1.0
	v_fmac_f32_e32 v37, v39, v37
	v_mul_f32_e32 v39, v38, v37
	v_fma_f32 v40, -v36, v39, v38
	v_fmac_f32_e32 v39, v40, v37
	v_fma_f32 v36, -v36, v39, v38
	v_div_fmas_f32 v36, v36, v37, v39
	v_div_fixup_f32 v64, v36, v35, 1.0
	v_pk_mul_f32 v[74:75], v[74:75], v[64:65] op_sel_hi:[1,0]
	v_pk_mul_f32 v[120:121], v[120:121], v[64:65] op_sel_hi:[1,0]
	v_pk_mul_f32 v[38:39], v[12:13], v[74:75]
	v_pk_fma_f32 v[74:75], v[146:147], v[74:75], v[78:79]
	v_xor_b32_e32 v79, 0x80000000, v5
	v_xor_b32_e32 v78, 0x80000000, v4
	v_pk_mul_f32 v[124:125], v[124:125], v[64:65] op_sel_hi:[1,0]
	v_pk_fma_f32 v[78:79], v[78:79], v[120:121], v[82:83]
	v_xor_b32_e32 v83, 0x80000000, v9
	v_xor_b32_e32 v82, 0x80000000, v8
	v_pk_mul_f32 v[128:129], v[128:129], v[64:65] op_sel_hi:[1,0]
	v_pk_fma_f32 v[82:83], v[82:83], v[124:125], v[86:87]
	v_xor_b32_e32 v87, 0x80000000, v17
	v_xor_b32_e32 v86, 0x80000000, v16
	v_pk_mul_f32 v[132:133], v[132:133], v[64:65] op_sel_hi:[1,0]
	v_pk_fma_f32 v[86:87], v[86:87], v[128:129], v[90:91]
	v_xor_b32_e32 v91, 0x80000000, v21
	v_xor_b32_e32 v90, 0x80000000, v20
	v_pk_mul_f32 v[136:137], v[136:137], v[64:65] op_sel_hi:[1,0]
	v_pk_fma_f32 v[90:91], v[90:91], v[132:133], v[94:95]
	v_xor_b32_e32 v95, 0x80000000, v25
	v_xor_b32_e32 v94, 0x80000000, v24
	v_pk_mul_f32 v[140:141], v[140:141], v[64:65] op_sel_hi:[1,0]
	v_pk_fma_f32 v[94:95], v[94:95], v[136:137], v[98:99]
	v_xor_b32_e32 v99, 0x80000000, v29
	v_xor_b32_e32 v98, 0x80000000, v28
	v_pk_mul_f32 v[104:105], v[104:105], v[64:65] op_sel_hi:[1,0]
	v_pk_mul_f32 v[118:119], v[118:119], v[64:65] op_sel_hi:[1,0]
	v_pk_mul_f32 v[122:123], v[122:123], v[64:65] op_sel_hi:[1,0]
	v_pk_mul_f32 v[126:127], v[126:127], v[64:65] op_sel_hi:[1,0]
	v_pk_mul_f32 v[130:131], v[130:131], v[64:65] op_sel_hi:[1,0]
	v_pk_mul_f32 v[134:135], v[134:135], v[64:65] op_sel_hi:[1,0]
	v_pk_mul_f32 v[138:139], v[138:139], v[64:65] op_sel_hi:[1,0]
	v_pk_mul_f32 v[142:143], v[142:143], v[64:65] op_sel_hi:[1,0]
	v_pk_mul_f32 v[144:145], v[144:145], v[64:65] op_sel_hi:[1,0]
	v_pk_fma_f32 v[98:99], v[98:99], v[140:141], v[102:103]
	v_xor_b32_e32 v103, 0x80000000, v33
	v_xor_b32_e32 v102, 0x80000000, v32
	v_pk_mul_f32 v[36:37], v[10:11], v[104:105]
	v_pk_mul_f32 v[42:43], v[4:5], v[120:121]
	v_pk_mul_f32 v[40:41], v[2:3], v[118:119]
	v_pk_mul_f32 v[46:47], v[8:9], v[124:125]
	v_pk_mul_f32 v[44:45], v[6:7], v[122:123]
	v_pk_mul_f32 v[50:51], v[16:17], v[128:129]
	v_pk_mul_f32 v[48:49], v[14:15], v[126:127]
	v_pk_mul_f32 v[54:55], v[20:21], v[132:133]
	v_pk_mul_f32 v[52:53], v[18:19], v[130:131]
	v_pk_mul_f32 v[58:59], v[24:25], v[136:137]
	v_pk_mul_f32 v[56:57], v[22:23], v[134:135]
	v_pk_mul_f32 v[62:63], v[28:29], v[140:141]
	v_pk_mul_f32 v[60:61], v[26:27], v[138:139]
	v_pk_mul_f32 v[66:67], v[32:33], v[144:145]
	v_pk_mul_f32 v[64:65], v[30:31], v[142:143]
	v_pk_fma_f32 v[76:77], v[10:11], v[104:105], v[76:77] neg_lo:[1,0,0] neg_hi:[1,0,0]
	v_pk_fma_f32 v[80:81], v[2:3], v[118:119], v[80:81] neg_lo:[1,0,0] neg_hi:[1,0,0]
	v_pk_fma_f32 v[84:85], v[6:7], v[122:123], v[84:85] neg_lo:[1,0,0] neg_hi:[1,0,0]
	v_pk_fma_f32 v[88:89], v[14:15], v[126:127], v[88:89] neg_lo:[1,0,0] neg_hi:[1,0,0]
	v_pk_fma_f32 v[92:93], v[18:19], v[130:131], v[92:93] neg_lo:[1,0,0] neg_hi:[1,0,0]
	v_pk_fma_f32 v[96:97], v[22:23], v[134:135], v[96:97] neg_lo:[1,0,0] neg_hi:[1,0,0]
	v_pk_fma_f32 v[100:101], v[26:27], v[138:139], v[100:101] neg_lo:[1,0,0] neg_hi:[1,0,0]
	v_pk_fma_f32 v[102:103], v[102:103], v[144:145], v[116:117]
	v_pk_fma_f32 v[104:105], v[30:31], v[142:143], v[114:115] neg_lo:[1,0,0] neg_hi:[1,0,0]
	v_mov_b32_e32 v35, v1

; template <bool SB> __device__ __forceinline__ void load_row(const void* xin, size_t row, int lane, f32x4 (&v)[8]) {
;     if (SB) { typedef _Float16 h16x4_t __attribute__((ext_vector_type(4))); const h16x4_t* xr = (const h16x4_t*)((const bf16*)xin + row * DM) + lane;
; #pragma unroll
;         for (int q = 0; q < 8; ++q) { const h16x4_t w = xr[64 * q]; v[q] = (f32x4){(float)w[0], (float)w[1], (float)w[2], (float)w[3]}; } }
;     ...
;             f32x4 v[8]; float ss = 0.f; load_row<SB>(xin, (size_t)row, lane, v);
; #pragma unroll
;             for (int q = 0; q < 8; ++q) ss += (v[q].x * v[q].x + v[q].y * v[q].y) + (v[q].z * v[q].z + v[q].w * v[q].w);
;             const float rstd = 1.0f / sqrtf(wave_sum(ss) * (1.0f / DM) + NORM_EPS);
.LBB0_4703:
	global_load_dwordx2 v[56:57], v[38:39], off offset:-2048
	global_load_dwordx2 v[58:59], v[38:39], off offset:-1536
	global_load_dwordx2 v[60:61], v[38:39], off offset:-1024
	global_load_dwordx2 v[62:63], v[38:39], off offset:-512
	global_load_dwordx2 v[64:65], v[38:39], off
	global_load_dwordx2 v[66:67], v[38:39], off offset:512
	global_load_dwordx2 v[68:69], v[38:39], off offset:1024
	global_load_dwordx2 v[70:71], v[38:39], off offset:1536
	s_waitcnt vmcnt(7)
	v_cvt_f32_f16_sdwa v73, v56 dst_sel:DWORD dst_unused:UNUSED_PAD src0_sel:WORD_1
	v_cvt_f32_f16_sdwa v75, v57 dst_sel:DWORD dst_unused:UNUSED_PAD src0_sel:WORD_1
	v_cvt_f32_f16_e32 v74, v57
	s_waitcnt vmcnt(6)
	v_cvt_f32_f16_sdwa v57, v58 dst_sel:DWORD dst_unused:UNUSED_PAD src0_sel:WORD_1
	v_cvt_f32_f16_sdwa v77, v59 dst_sel:DWORD dst_unused:UNUSED_PAD src0_sel:WORD_1
	v_cvt_f32_f16_e32 v72, v56
	v_cvt_f32_f16_e32 v56, v58
	v_cvt_f32_f16_e32 v76, v59
	s_waitcnt vmcnt(5)
	v_cvt_f32_f16_sdwa v59, v60 dst_sel:DWORD dst_unused:UNUSED_PAD src0_sel:WORD_1
	v_cvt_f32_f16_sdwa v79, v61 dst_sel:DWORD dst_unused:UNUSED_PAD src0_sel:WORD_1
	v_cvt_f32_f16_e32 v58, v60
	v_cvt_f32_f16_e32 v78, v61
	s_waitcnt vmcnt(4)
	v_cvt_f32_f16_sdwa v61, v62 dst_sel:DWORD dst_unused:UNUSED_PAD src0_sel:WORD_1
	v_cvt_f32_f16_sdwa v81, v63 dst_sel:DWORD dst_unused:UNUSED_PAD src0_sel:WORD_1
	v_cvt_f32_f16_e32 v60, v62
	v_cvt_f32_f16_e32 v80, v63
	s_waitcnt vmcnt(3)
	v_cvt_f32_f16_sdwa v63, v64 dst_sel:DWORD dst_unused:UNUSED_PAD src0_sel:WORD_1
	v_cvt_f32_f16_e32 v62, v64
	v_cvt_f32_f16_sdwa v83, v65 dst_sel:DWORD dst_unused:UNUSED_PAD src0_sel:WORD_1
	v_cvt_f32_f16_e32 v82, v65
	v_mov_b32_e32 v90, v73
	v_mov_b32_e32 v91, v57
	v_mov_b32_e32 v94, v75
	v_mov_b32_e32 v95, v77
	s_waitcnt vmcnt(2)
	v_cvt_f32_f16_sdwa v65, v66 dst_sel:DWORD dst_unused:UNUSED_PAD src0_sel:WORD_1
	v_cvt_f32_f16_e32 v64, v66
	v_cvt_f32_f16_sdwa v85, v67 dst_sel:DWORD dst_unused:UNUSED_PAD src0_sel:WORD_1
	v_cvt_f32_f16_e32 v84, v67
	s_waitcnt vmcnt(1)
	v_cvt_f32_f16_sdwa v67, v68 dst_sel:DWORD dst_unused:UNUSED_PAD src0_sel:WORD_1
	v_cvt_f32_f16_e32 v66, v68
	v_cvt_f32_f16_sdwa v87, v69 dst_sel:DWORD dst_unused:UNUSED_PAD src0_sel:WORD_1
	v_cvt_f32_f16_e32 v86, v69
	s_waitcnt vmcnt(0)
	v_cvt_f32_f16_sdwa v69, v70 dst_sel:DWORD dst_unused:UNUSED_PAD src0_sel:WORD_1
	v_cvt_f32_f16_e32 v68, v70
	v_cvt_f32_f16_sdwa v89, v71 dst_sel:DWORD dst_unused:UNUSED_PAD src0_sel:WORD_1
	v_cvt_f32_f16_e32 v88, v71
	v_mov_b32_e32 v70, v72
	v_mov_b32_e32 v71, v56
	v_mov_b32_e32 v92, v74
	v_mov_b32_e32 v93, v76
	v_mov_b32_e32 v98, v59
	v_mov_b32_e32 v99, v79
	v_pk_mul_f32 v[90:91], v[90:91], v[90:91]
	v_pk_mul_f32 v[94:95], v[94:95], v[94:95]
	v_mov_b32_e32 v96, v58
	v_mov_b32_e32 v97, v78
	v_pk_mul_f32 v[98:99], v[98:99], v[98:99]
	v_pk_fma_f32 v[70:71], v[70:71], v[70:71], v[90:91]
	v_pk_fma_f32 v[90:91], v[92:93], v[92:93], v[94:95]
	v_mul_f32_e32 v100, v61, v61
	v_mul_f32_e32 v102, v81, v81
	v_pk_fma_f32 v[92:93], v[96:97], v[96:97], v[98:99]
	v_pk_add_f32 v[70:71], v[70:71], v[90:91]
	v_pk_mul_f32 v[104:105], v[62:63], v[62:63]
	v_pk_mul_f32 v[106:107], v[82:83], v[82:83]
	v_pk_fma_f32 v[100:101], v[60:61], v[60:61], v[100:101] op_sel_hi:[1,1,0]
	v_pk_fma_f32 v[102:103], v[80:81], v[80:81], v[102:103] op_sel_hi:[1,1,0]
	v_pk_add_f32 v[90:91], v[92:93], v[92:93] op_sel:[0,1] op_sel_hi:[1,0]
	v_pk_add_f32 v[70:71], v[70:71], v[70:71] op_sel:[0,1] op_sel_hi:[1,0]
	v_mov_b32_e32 v110, v65
	v_mov_b32_e32 v111, v85
	v_mov_b32_e32 v101, v106
	v_mov_b32_e32 v103, v107
	v_mov_b32_e32 v91, v105
	v_mov_b32_e32 v71, v104
	v_mov_b32_e32 v108, v64
	v_mov_b32_e32 v109, v84
	v_pk_mul_f32 v[110:111], v[110:111], v[110:111]
	v_pk_add_f32 v[92:93], v[100:101], v[102:103]
	v_pk_add_f32 v[70:71], v[70:71], v[90:91]
	v_mul_f32_e32 v112, v67, v67
	v_mul_f32_e32 v114, v87, v87
	v_pk_fma_f32 v[94:95], v[108:109], v[108:109], v[110:111]
	v_pk_add_f32 v[70:71], v[70:71], v[92:93]
	v_pk_mul_f32 v[116:117], v[68:69], v[68:69]
	v_pk_mul_f32 v[118:119], v[88:89], v[88:89]
	v_pk_fma_f32 v[112:113], v[66:67], v[66:67], v[112:113] op_sel_hi:[1,1,0]
	v_pk_fma_f32 v[114:115], v[86:87], v[86:87], v[114:115] op_sel_hi:[1,1,0]
	v_pk_add_f32 v[94:95], v[94:95], v[94:95] op_sel:[0,1] op_sel_hi:[1,0]
	v_pk_add_f32 v[70:71], v[70:71], v[70:71] op_sel:[0,1] op_sel_hi:[1,0]
	v_mov_b32_e32 v113, v118
	v_mov_b32_e32 v115, v119
	v_mov_b32_e32 v95, v117
	v_mov_b32_e32 v71, v116
	v_pk_add_f32 v[96:97], v[112:113], v[114:115]
	v_pk_add_f32 v[70:71], v[70:71], v[94:95]
	s_nop 0
	v_pk_add_f32 v[70:71], v[70:71], v[96:97]
	s_nop 0
	v_add_f32_e32 v55, v70, v71
	s_nop 0
	s_waitcnt lgkmcnt(0)
	s_nop 1
	v_add_f32_dpp v55, v55, v55 quad_perm:[1,0,3,2] row_mask:0xf bank_mask:0xf bound_ctrl:1
	s_nop 0
	s_waitcnt lgkmcnt(0)
	s_nop 1
	v_add_f32_dpp v55, v55, v55 quad_perm:[2,3,0,1] row_mask:0xf bank_mask:0xf bound_ctrl:1
	s_nop 0
	s_waitcnt lgkmcnt(0)
	s_nop 1
	v_add_f32_dpp v55, v55, v55 row_half_mirror row_mask:0xf bank_mask:0xf bound_ctrl:1
	s_nop 0
	s_waitcnt lgkmcnt(0)
	s_nop 1
	v_add_f32_dpp v55, v55, v55 row_mirror row_mask:0xf bank_mask:0xf bound_ctrl:1
	s_nop 0
	s_waitcnt lgkmcnt(0)
	s_nop 1
	v_add_f32_dpp v55, v55, v55 row_bcast:15 row_mask:0xa bank_mask:0xf
	s_nop 0
	s_waitcnt lgkmcnt(0)
; __device__ __forceinline__ float wave_max(float v) {
; #pragma unroll
;     for (int o = 1; o < 64; o <<= 1) v = fmaxf(v, __shfl_xor(v, o));
;     return v;
; }
;     ...
;             const float rstd = 1.0f / sqrtf(wave_sum(ss) * (1.0f / DM) + NORM_EPS);
;             if (F8 == 2) { unsigned* o4 = (unsigned*)((unsigned char*)xn + (size_t)row * DM) + lane; float mx = 0.f;
; #pragma unroll
;                 for (int q = 0; q < 8; ++q) { v[q] = v[q] * rstd * gn[q]; mx = fmaxf(fmaxf(mx, fmaxf(fabsf(v[q].x), fabsf(v[q].y))), fmaxf(fabsf(v[q].z), fabsf(v[q].w))); }
;                 mx = fmaxf(wave_max(mx), 1e-30f); const float qs = 127.0f / mx;
	s_nop 1
	v_add_f32_dpp v55, v55, v55 row_bcast:31 row_mask:0xc bank_mask:0xf
	s_nop 0
	v_readlane_b32 s98, v55, 63
	s_nop 1
	v_mov_b32_e32 v55, s98
	v_fmamk_f32 v55, v55, 0x3a000000, v53
	v_mul_f32_e32 v70, 0x4f800000, v55
	v_cmp_gt_f32_e32 vcc, s7, v55
	s_nop 1
	v_cndmask_b32_e32 v55, v55, v70, vcc
	v_sqrt_f32_e32 v70, v55
	s_nop 0
	v_add_u32_e32 v71, -1, v70
	v_add_u32_e32 v90, 1, v70
	v_fma_f32 v91, -v71, v70, v55
	v_fma_f32 v92, -v90, v70, v55
	v_cmp_ge_f32_e64 s[2:3], 0, v91
	s_nop 1
	v_cndmask_b32_e64 v70, v70, v71, s[2:3]
	v_cmp_lt_f32_e64 s[2:3], 0, v92
	s_nop 1
	v_cndmask_b32_e64 v70, v70, v90, s[2:3]
	v_mul_f32_e32 v71, 0x37800000, v70
	v_cndmask_b32_e32 v70, v70, v71, vcc
	v_cmp_class_f32_e32 vcc, v55, v54
	s_nop 1
	v_cndmask_b32_e32 v55, v70, v55, vcc
	v_div_scale_f32 v70, s[2:3], v55, v55, 1.0
	v_rcp_f32_e32 v71, v70
	v_div_scale_f32 v90, vcc, 1.0, v55, 1.0
	v_fma_f32 v91, -v70, v71, 1.0
	v_fmac_f32_e32 v71, v91, v71
	v_mul_f32_e32 v91, v90, v71
	v_fma_f32 v92, -v70, v91, v90
	v_fmac_f32_e32 v91, v92, v71
	v_fma_f32 v70, -v70, v91, v90
	v_div_fmas_f32 v70, v70, v71, v91
	v_div_fixup_f32 v70, v70, v55, 1.0
	v_pk_mul_f32 v[74:75], v[74:75], v[70:71] op_sel_hi:[1,0]
	v_pk_mul_f32 v[72:73], v[72:73], v[70:71] op_sel_hi:[1,0]
	v_pk_mul_f32 v[74:75], v[12:13], v[74:75]
	v_pk_mul_f32 v[56:57], v[56:57], v[70:71] op_sel_hi:[1,0]
	v_pk_mul_f32 v[76:77], v[76:77], v[70:71] op_sel_hi:[1,0]
	v_pk_mul_f32 v[58:59], v[58:59], v[70:71] op_sel_hi:[1,0]
	v_pk_mul_f32 v[78:79], v[78:79], v[70:71] op_sel_hi:[1,0]
	v_pk_mul_f32 v[60:61], v[60:61], v[70:71] op_sel_hi:[1,0]
	v_pk_mul_f32 v[80:81], v[80:81], v[70:71] op_sel_hi:[1,0]
	v_pk_mul_f32 v[72:73], v[10:11], v[72:73]
	v_max_f32_e64 v71, |v74|, |v75|
	v_pk_mul_f32 v[76:77], v[4:5], v[76:77]
	v_pk_mul_f32 v[56:57], v[2:3], v[56:57]
	v_max_f32_e64 v55, |v72|, |v73|
	v_pk_mul_f32 v[62:63], v[62:63], v[70:71] op_sel_hi:[1,0]
	v_pk_mul_f32 v[78:79], v[8:9], v[78:79]
	v_pk_mul_f32 v[58:59], v[6:7], v[58:59]
	v_max_f32_e64 v90, |v56|, |v57|
	v_max_f32_e64 v91, |v76|, |v77|
	v_max3_f32 v55, v55, 0, v71
	v_pk_mul_f32 v[62:63], v[18:19], v[62:63]
	v_pk_mul_f32 v[80:81], v[16:17], v[80:81]
	v_pk_mul_f32 v[60:61], v[14:15], v[60:61]
	v_max_f32_e64 v92, |v58|, |v59|
	v_max_f32_e64 v93, |v78|, |v79|
	v_max3_f32 v55, v55, v90, v91
	v_pk_mul_f32 v[82:83], v[82:83], v[70:71] op_sel_hi:[1,0]
	v_max_f32_e64 v71, |v62|, |v63|
	v_max_f32_e64 v94, |v60|, |v61|
	v_max_f32_e64 v95, |v80|, |v81|
	v_max3_f32 v55, v55, v92, v93
	v_pk_mul_f32 v[82:83], v[20:21], v[82:83]
	v_pk_mul_f32 v[64:65], v[64:65], v[70:71] op_sel_hi:[1,0]
	v_max3_f32 v55, v55, v94, v95
	v_max_f32_e64 v90, |v82|, |v83|
	v_pk_mul_f32 v[64:65], v[22:23], v[64:65]
	v_max3_f32 v55, v55, v71, v90
	v_pk_mul_f32 v[84:85], v[84:85], v[70:71] op_sel_hi:[1,0]
	v_max_f32_e64 v71, |v64|, |v65|
	v_pk_mul_f32 v[84:85], v[24:25], v[84:85]
	v_pk_mul_f32 v[66:67], v[66:67], v[70:71] op_sel_hi:[1,0]
	v_pk_mul_f32 v[86:87], v[86:87], v[70:71] op_sel_hi:[1,0]
	v_max_f32_e64 v90, |v84|, |v85|
	v_pk_mul_f32 v[86:87], v[28:29], v[86:87]
	v_pk_mul_f32 v[66:67], v[26:27], v[66:67]
	v_max3_f32 v55, v55, v71, v90
	v_max_f32_e64 v71, |v66|, |v67|
	v_max_f32_e64 v90, |v86|, |v87|
	v_max3_f32 v55, v55, v71, v90
	v_pk_mul_f32 v[68:69], v[68:69], v[70:71] op_sel_hi:[1,0]
	v_pk_mul_f32 v[70:71], v[88:89], v[70:71] op_sel_hi:[1,0]
	v_pk_mul_f32 v[68:69], v[30:31], v[68:69]
	v_pk_mul_f32 v[70:71], v[32:33], v[70:71]
	v_max_f32_e64 v88, |v68|, |v69|
	v_max_f32_e64 v89, |v70|, |v71|
	v_max3_f32 v55, v55, v88, v89
	s_nop 0
	s_waitcnt lgkmcnt(0)
	s_nop 0
	s_nop 1
	v_max_f32_dpp v55, v55, v55 quad_perm:[1,0,3,2] row_mask:0xf bank_mask:0xf bound_ctrl:1
	s_nop 0
	s_waitcnt lgkmcnt(0)
	s_nop 0
	s_nop 1
	v_max_f32_dpp v55, v55, v55 quad_perm:[2,3,0,1] row_mask:0xf bank_mask:0xf bound_ctrl:1
	s_nop 0
	s_waitcnt lgkmcnt(0)
	s_nop 0
	s_nop 1
	v_max_f32_dpp v55, v55, v55 row_half_mirror row_mask:0xf bank_mask:0xf bound_ctrl:1
	s_nop 0
	s_waitcnt lgkmcnt(0)
	s_nop 0
	s_nop 1
	v_max_f32_dpp v55, v55, v55 row_mirror row_mask:0xf bank_mask:0xf bound_ctrl:1
	s_nop 0
	s_waitcnt lgkmcnt(0)
	s_nop 0
	s_nop 1
	v_max_f32_dpp v55, v55, v55 row_bcast:15 row_mask:0xa bank_mask:0xf
	s_nop 0
	s_waitcnt lgkmcnt(0)
;     ...
;                 mx = fmaxf(wave_max(mx), 1e-30f); const float qs = 127.0f / mx;
; #pragma unroll
;                 for (int q = 0; q < 8; ++q) o4[64 * q] = pack_i8x4(v[q].x * qs, v[q].y * qs, v[q].z * qs, v[q].w * qs);
;                 if (lane == 0) ((float*)(ws + WS_ROWQ))[row] = mx * (1.0f / 127.0f); }
	s_nop 1
	v_max_f32_dpp v55, v55, v55 row_bcast:31 row_mask:0xc bank_mask:0xf
	s_nop 0
	v_readlane_b32 s98, v55, 63
	s_nop 1
	v_mov_b32_e32 v55, s98
	v_max_f32_e32 v55, s8, v55
	v_div_scale_f32 v88, s[2:3], v55, v55, s9
	v_rcp_f32_e32 v89, v88
	v_div_scale_f32 v90, vcc, s9, v55, s9
	v_fma_f32 v91, -v88, v89, 1.0
	v_fmac_f32_e32 v89, v91, v89
	v_mul_f32_e32 v91, v90, v89
	v_fma_f32 v92, -v88, v91, v90
	v_fmac_f32_e32 v91, v92, v89
	v_fma_f32 v88, -v88, v91, v90
	v_div_fmas_f32 v88, v88, v89, v91
	v_div_fixup_f32 v88, v88, v55, s9
	v_mul_f32_e32 v73, v73, v88
	v_mul_f32_e32 v72, v72, v88
	v_mul_f32_e32 v74, v74, v88
	v_mul_f32_e32 v75, v75, v88
	v_rndne_f32_e32 v73, v73
	v_rndne_f32_e32 v72, v72
	v_cvt_i32_f32_e32 v73, v73
	v_rndne_f32_e32 v74, v74
	v_rndne_f32_e32 v75, v75
	v_cvt_i32_f32_e32 v72, v72
	v_cvt_i32_f32_sdwa v74, v74 dst_sel:WORD_1 dst_unused:UNUSED_PAD src0_sel:DWORD
	v_cvt_i32_f32_e32 v75, v75
	v_lshlrev_b32_e32 v73, 8, v73
	v_and_b32_e32 v73, 0xff00, v73
	v_and_b32_e32 v74, 0xff0000, v74
	v_perm_b32 v72, v75, v72, s10
	v_or3_b32 v72, v72, v73, v74
	v_mul_f32_e32 v57, v57, v88
	global_store_dword v[42:43], v72, off offset:-1024
	v_mul_f32_e32 v56, v56, v88
	v_mul_f32_e32 v72, v76, v88
	v_mul_f32_e32 v73, v77, v88
	v_rndne_f32_e32 v57, v57
	v_rndne_f32_e32 v56, v56
	v_cvt_i32_f32_e32 v57, v57
	v_rndne_f32_e32 v72, v72
	v_rndne_f32_e32 v73, v73
	v_cvt_i32_f32_e32 v56, v56
	v_cvt_i32_f32_sdwa v72, v72 dst_sel:WORD_1 dst_unused:UNUSED_PAD src0_sel:DWORD
	v_cvt_i32_f32_e32 v73, v73
	v_lshlrev_b32_e32 v57, 8, v57
	v_and_b32_e32 v57, 0xff00, v57
	v_and_b32_e32 v72, 0xff0000, v72
	v_perm_b32 v56, v73, v56, s10
	v_or3_b32 v56, v56, v57, v72
	v_mul_f32_e32 v57, v59, v88
	global_store_dword v[42:43], v56, off offset:-768
	v_mul_f32_e32 v56, v58, v88
	v_mul_f32_e32 v58, v78, v88
	v_mul_f32_e32 v59, v79, v88
	v_rndne_f32_e32 v57, v57
	v_rndne_f32_e32 v56, v56
	v_cvt_i32_f32_e32 v57, v57
	v_rndne_f32_e32 v58, v58
	v_rndne_f32_e32 v59, v59
	v_cvt_i32_f32_e32 v56, v56
	v_cvt_i32_f32_sdwa v58, v58 dst_sel:WORD_1 dst_unused:UNUSED_PAD src0_sel:DWORD
	v_cvt_i32_f32_e32 v59, v59
	v_lshlrev_b32_e32 v57, 8, v57
	v_and_b32_e32 v57, 0xff00, v57
	v_and_b32_e32 v58, 0xff0000, v58
	v_perm_b32 v56, v59, v56, s10
	v_or3_b32 v56, v56, v57, v58
	v_mul_f32_e32 v57, v61, v88
	global_store_dword v[42:43], v56, off offset:-512
	v_mul_f32_e32 v56, v60, v88
	v_mul_f32_e32 v58, v80, v88
	v_mul_f32_e32 v59, v81, v88
	v_rndne_f32_e32 v57, v57
	v_rndne_f32_e32 v56, v56
	v_cvt_i32_f32_e32 v57, v57
	v_rndne_f32_e32 v58, v58
	v_rndne_f32_e32 v59, v59
	v_cvt_i32_f32_e32 v56, v56
	v_cvt_i32_f32_sdwa v58, v58 dst_sel:WORD_1 dst_unused:UNUSED_PAD src0_sel:DWORD
	v_cvt_i32_f32_e32 v59, v59
	v_lshlrev_b32_e32 v57, 8, v57
	v_and_b32_e32 v57, 0xff00, v57
	v_and_b32_e32 v58, 0xff0000, v58
	v_perm_b32 v56, v59, v56, s10
	v_or3_b32 v56, v56, v57, v58
	v_mul_f32_e32 v57, v63, v88
	global_store_dword v[42:43], v56, off offset:-256
	v_mul_f32_e32 v56, v62, v88
	v_mul_f32_e32 v58, v82, v88
	v_mul_f32_e32 v59, v83, v88
	v_rndne_f32_e32 v57, v57
	v_rndne_f32_e32 v56, v56
	v_cvt_i32_f32_e32 v57, v57
	v_rndne_f32_e32 v58, v58
	v_rndne_f32_e32 v59, v59
	v_cvt_i32_f32_e32 v56, v56
	v_cvt_i32_f32_sdwa v58, v58 dst_sel:WORD_1 dst_unused:UNUSED_PAD src0_sel:DWORD
	v_cvt_i32_f32_e32 v59, v59
	v_lshlrev_b32_e32 v57, 8, v57
	v_and_b32_e32 v57, 0xff00, v57
	v_and_b32_e32 v58, 0xff0000, v58
	v_perm_b32 v56, v59, v56, s10
	v_or3_b32 v56, v56, v57, v58
	v_mul_f32_e32 v57, v65, v88
	global_store_dword v[42:43], v56, off
	v_mul_f32_e32 v56, v64, v88
	v_mul_f32_e32 v58, v84, v88
	v_mul_f32_e32 v59, v85, v88
	v_rndne_f32_e32 v57, v57
	v_rndne_f32_e32 v56, v56
	v_cvt_i32_f32_e32 v57, v57
	v_rndne_f32_e32 v58, v58
	v_rndne_f32_e32 v59, v59
	v_cvt_i32_f32_e32 v56, v56
	v_cvt_i32_f32_sdwa v58, v58 dst_sel:WORD_1 dst_unused:UNUSED_PAD src0_sel:DWORD
	v_cvt_i32_f32_e32 v59, v59
	v_lshlrev_b32_e32 v57, 8, v57
	v_and_b32_e32 v57, 0xff00, v57
	v_and_b32_e32 v58, 0xff0000, v58
	v_perm_b32 v56, v59, v56, s10
	v_or3_b32 v56, v56, v57, v58
	v_mul_f32_e32 v57, v67, v88
	global_store_dword v[42:43], v56, off offset:256
	v_mul_f32_e32 v56, v66, v88
	v_mul_f32_e32 v58, v86, v88
	v_mul_f32_e32 v59, v87, v88
	v_rndne_f32_e32 v57, v57
	v_rndne_f32_e32 v56, v56
	v_cvt_i32_f32_e32 v57, v57
	v_rndne_f32_e32 v58, v58
	v_rndne_f32_e32 v59, v59
	v_cvt_i32_f32_e32 v56, v56
	v_cvt_i32_f32_sdwa v58, v58 dst_sel:WORD_1 dst_unused:UNUSED_PAD src0_sel:DWORD
	v_cvt_i32_f32_e32 v59, v59
	v_lshlrev_b32_e32 v57, 8, v57
	v_and_b32_e32 v57, 0xff00, v57
	v_and_b32_e32 v58, 0xff0000, v58
	v_perm_b32 v56, v59, v56, s10
	v_or3_b32 v56, v56, v57, v58
	v_mul_f32_e32 v57, v69, v88
	global_store_dword v[42:43], v56, off offset:512
	v_mul_f32_e32 v56, v68, v88
	v_mul_f32_e32 v58, v70, v88
	v_mul_f32_e32 v59, v71, v88
	v_rndne_f32_e32 v57, v57
	v_rndne_f32_e32 v56, v56
	v_cvt_i32_f32_e32 v57, v57
	v_rndne_f32_e32 v58, v58
	v_rndne_f32_e32 v59, v59
	v_cvt_i32_f32_e32 v56, v56
	v_cvt_i32_f32_sdwa v58, v58 dst_sel:WORD_1 dst_unused:UNUSED_PAD src0_sel:DWORD
	v_cvt_i32_f32_e32 v59, v59
	v_lshlrev_b32_e32 v57, 8, v57
	v_and_b32_e32 v57, 0xff00, v57
	v_and_b32_e32 v58, 0xff0000, v58
	v_perm_b32 v56, v59, v56, s10
	v_or3_b32 v56, v56, v57, v58
	global_store_dword v[42:43], v56, off offset:768
	s_and_saveexec_b64 s[2:3], s[0:1]
	s_cbranch_execz .LBB0_4702
	v_mul_f32_e32 v55, 0x3c010204, v55
	global_store_dword v[46:47], v55, off
	s_branch .LBB0_4702
